# speedup vs baseline: 1.0351x; 1.0081x over previous
.LBB3_18:
	s_or_b64 exec, exec, s[4:5]
	v_and_b32_e32 v188, 15, v0
	v_lshrrev_b32_e32 v239, 6, v0
	v_bfe_u32 v189, v0, 4, 2
	v_mov_b32_e32 v179, 0
	v_lshlrev_b32_e32 v238, 8, v188
	v_lshlrev_b32_e32 v178, 23, v239
	s_lshl_b64 s[2:3], s[2:3], 14
	s_waitcnt vmcnt(0)
	v_lshl_or_b32 v12, v189, 3, v238
	s_waitcnt lgkmcnt(0)
	s_add_u32 s54, s20, s50
	s_addc_u32 s55, s21, s51
	s_add_u32 s56, s42, s50
	s_addc_u32 s57, s43, s51
	s_add_u32 s60, s40, s50
	s_addc_u32 s61, s41, s51
	s_load_dword s58, s[54:55], 0x0
	s_load_dword s59, s[54:55], 0x400
	s_load_dword s62, s[56:57], 0x0
	s_load_dword s63, s[56:57], 0x400
	s_load_dword s64, s[60:61], 0x0
	s_load_dword s65, s[60:61], 0x400
	s_load_dword s66, s[46:47], 0x400
	s_load_dwordx2 s[68:69], s[0:1], 0x38
	v_lshl_add_u64 v[10:11], s[16:17], 0, v[178:179]
	v_lshl_add_u64 v[74:75], v[10:11], 0, s[2:3]
	v_lshlrev_b32_e32 v178, 2, v12
	v_lshl_add_u64 v[46:47], v[74:75], 0, v[178:179]
	s_barrier
	global_load_dwordx4 v[66:69], v[46:47], off offset:16
	global_load_dwordx4 v[70:73], v[46:47], off
	global_load_dwordx4 v[38:41], v[46:47], off offset:144
	global_load_dwordx4 v[62:65], v[46:47], off offset:128
	global_load_dwordx4 v[30:33], v[46:47], off offset:272
	global_load_dwordx4 v[34:37], v[46:47], off offset:256
	global_load_dwordx4 v[22:25], v[46:47], off offset:400
	global_load_dwordx4 v[26:29], v[46:47], off offset:384
	global_load_dwordx4 v[14:17], v[46:47], off offset:528
	global_load_dwordx4 v[18:21], v[46:47], off offset:512
	global_load_dwordx4 v[58:61], v[46:47], off offset:656
	global_load_dwordx4 v[10:13], v[46:47], off offset:640
	global_load_dwordx4 v[50:53], v[46:47], off offset:784
	global_load_dwordx4 v[54:57], v[46:47], off offset:768
	global_load_dwordx4 v[42:45], v[46:47], off offset:912
	s_nop 0
	global_load_dwordx4 v[46:49], v[46:47], off offset:896
	v_lshl_add_u32 v76, v0, 3, 0
	v_add_u32_e32 v197, 0x11000, v76
	v_mov_b32_e32 v76, 0x3fb8aa3b
	v_mul_f32_e32 v77, s10, v76
	v_rndne_f32_e32 v78, v77
	v_sub_f32_e32 v79, v77, v78
	v_fma_f32 v76, s10, v76, -v77
	v_mov_b32_e32 v77, 0x32a5705f
	v_fmac_f32_e32 v76, s10, v77
	v_add_f32_e32 v76, v79, v76
	v_exp_f32_e32 v76, v76
	v_cvt_i32_f32_e32 v77, v78
	v_mov_b32_e32 v80, 0x7f800000
	v_and_b32_e32 v97, 63, v0
	s_add_i32 s2, 0, 0x12000
	v_ldexp_f32 v76, v76, v77
	v_mov_b32_e32 v77, 0xc2ce8ed0
	v_cmp_nlt_f32_e32 vcc, s10, v77
	v_mov_b32_e32 v77, 0x42b17218
	v_lshl_add_u32 v196, v97, 2, s2
	v_cndmask_b32_e32 v76, 0, v76, vcc
	v_cmp_ngt_f32_e32 vcc, s10, v77
	s_mov_b32 s2, 0x800000
	v_mov_b32_e32 v77, 0x42000000
	v_cndmask_b32_e32 v76, v80, v76, vcc
	v_mul_f32_e32 v76, 0x41000000, v76
	v_cmp_gt_f32_e32 vcc, s2, v76
	s_and_b64 s[2:3], vcc, exec
	s_cselect_b32 s2, 32, 0
	v_ldexp_f32 v76, v76, s2
	v_log_f32_e32 v76, v76
	v_cndmask_b32_e32 v77, 0, v77, vcc
	s_mov_b32 s2, 0xc2fc0000
	v_lshlrev_b32_e32 v83, 1, v0
	v_sub_f32_e32 v76, v76, v77
	v_rndne_f32_e32 v76, v76
	v_mov_b32_e32 v77, 0x42800000
	v_cmp_gt_f32_e32 vcc, s2, v76
	s_and_b64 s[2:3], vcc, exec
	s_cselect_b32 s2, 0xffffffc0, 0
	v_cndmask_b32_e32 v77, 0, v77, vcc
	v_add_f32_e32 v76, v76, v77
	v_exp_f32_e32 v76, v76
	v_lshl_add_u32 v77, v97, 3, 0
	v_lshrrev_b32_e32 v94, 2, v0
	v_bfe_u32 v79, v0, 1, 2
	v_ldexp_f32 v82, v76, s2
	v_div_scale_f32 v76, s[2:3], v82, v82, 1.0
	v_rcp_f32_e32 v80, v76
	v_add_u32_e32 v192, 0x10000, v77
	v_lshrrev_b32_e32 v78, 1, v0
	v_and_or_b32 v198, v94, 12, v79
	v_fma_f32 v77, -v76, v80, 1.0
	v_and_b32_e32 v79, 2, v83
	v_fmac_f32_e32 v80, v77, v80
	v_div_scale_f32 v77, vcc, 1.0, v82, 1.0
	v_and_or_b32 v78, v78, 4, v79
	v_mul_f32_e32 v81, v77, v80
	v_lshlrev_b32_e32 v199, 1, v78
	v_fma_f32 v78, -v76, v81, v77
	v_fmac_f32_e32 v81, v78, v80
	ds_read_b64 v[86:87], v197
	ds_read_b64 v[78:79], v192
	v_fma_f32 v76, -v76, v81, v77
	v_div_fmas_f32 v76, v76, v80, v81
	v_div_fixup_f32 v95, v76, v82, 1.0
	ds_read2st64_b32 v[76:77], v196 offset0:2 offset1:3
	ds_read2st64_b32 v[80:81], v196 offset0:4 offset1:5
	s_waitcnt lgkmcnt(2)
	v_pk_mul_f32 v[84:85], v[86:87], v[78:79] op_sel:[0,1]
	v_lshlrev_b32_e32 v96, 3, v239
	v_pk_fma_f32 v[90:91], v[86:87], v[78:79], v[84:85] op_sel:[1,0,0] op_sel_hi:[0,0,1]
	v_pk_fma_f32 v[92:93], v[86:87], v[78:79], v[84:85] op_sel:[1,0,0] op_sel_hi:[0,0,1] neg_lo:[0,0,1] neg_hi:[0,0,1]
	s_waitcnt lgkmcnt(1)
	v_mul_f32_e32 v78, v77, v90
	v_fma_f32 v92, v76, v93, -v78
	v_cmp_lt_u32_e64 s[6:7], 63, v0
	v_add_u32_e32 v200, -1, v96
	v_pk_mov_b32 v[88:89], v[86:87], v[86:87] op_sel:[1,0]
	s_and_saveexec_b64 s[2:3], s[6:7]
	s_cbranch_execz .LBB3_20
	v_mov_b32_e32 v91, v93
	v_pk_mul_f32 v[78:79], v[76:77], v[90:91]
	v_bitop3_b32 v84, v200, v198, 15 bitop3:0x6c
	v_add_f32_e32 v78, v78, v79
	v_mul_f32_e32 v79, v95, v92
	v_mul_f32_e64 v78, v95, -v78
	v_cvt_pk_f16_f32 v78, v79, v78
	v_lshl_add_u32 v79, v200, 8, 0
	v_lshlrev_b32_e32 v84, 4, v84
	v_add3_u32 v79, v79, v84, v199
	ds_write_b32 v79, v78 offset:32768

.LBB3_24:
	s_or_b64 exec, exec, s[2:3]
	v_lshrrev_b32_e32 v82, 3, v0
	v_lshlrev_b32_e32 v78, 3, v0
	s_movk_i32 s2, 0x70
	v_and_b32_e32 v83, 56, v78
	v_not_b32_e32 v78, v82
	v_bitop3_b32 v85, v191, s2, v0 bitop3:0x48
	s_mov_b64 s[2:3], 0x400000
	v_lshlrev_b32_e32 v78, 2, v78
	v_lshl_add_u64 v[182:183], v[74:75], 0, s[2:3]
	v_lshlrev_b32_e32 v74, 2, v83
	v_add3_u32 v74, s30, v78, v74
	v_sub_co_u32_e32 v78, vcc, v82, v83
	v_lshlrev_b32_e32 v122, 14, v239
	v_mov_b32_e32 v123, 0
	v_add_u32_e32 v75, 0x100, v74
	v_lshl_add_u32 v78, v78, 2, s30
	v_or_b32_e32 v86, 1, v83
	s_waitcnt lgkmcnt(0)
	v_lshl_add_u64 v[76:77], s[18:19], 0, v[122:123]
	v_mov_b32_e32 v179, v123
	v_cndmask_b32_e32 v227, v78, v75, vcc
	v_sub_u32_e32 v78, v82, v86
	v_lshl_add_u32 v78, v78, 2, s30
	v_add_u32_e32 v79, 0x104, v74
	v_cmp_lt_u32_e32 vcc, v83, v82
	v_lshl_add_u64 v[180:181], v[76:77], 0, v[178:179]
	v_or_b32_e32 v77, 2, v83
	v_cndmask_b32_e32 v228, v79, v78, vcc
	v_sub_co_u32_e32 v79, vcc, v82, v77
	s_add_i32 s18, 0, 0x10000
	v_add_u32_e32 v78, 0x108, v74
	v_lshl_add_u32 v79, v79, 2, s30
	v_or_b32_e32 v90, 3, v83
	s_add_u32 s2, s20, s50
	v_cndmask_b32_e32 v229, v79, v78, vcc
	v_sub_co_u32_e32 v78, vcc, v82, v90
	s_barrier
	s_addc_u32 s3, s21, s51
	v_lshl_add_u32 v91, v78, 2, s30
	global_load_dwordx4 v[78:81], v[180:181], off
	s_waitcnt lgkmcnt(0)
	s_mov_b32 s34, s58
	ds_read_b32 v75, v227
	ds_read_b32 v87, v228
	ds_read_b32 v88, v229
	v_lshlrev_b32_e32 v138, 7, v188
	v_lshl_add_u32 v84, v82, 7, s18
	v_add_u32_e32 v130, s18, v138
	s_waitcnt lgkmcnt(0)
	v_add_f32_e32 v76, s34, v75
	v_cmp_eq_u32_e64 s[18:19], v83, v82
	v_add_u32_e32 v89, 0x10c, v74
	v_cmp_eq_u32_e64 s[20:21], v82, v86
	v_cndmask_b32_e64 v75, v75, v76, s[18:19]
	v_add_f32_e32 v76, s34, v87
	v_or_b32_e32 v93, 4, v83
	v_cndmask_b32_e32 v230, v91, v89, vcc
	v_cndmask_b32_e64 v76, v87, v76, s[20:21]
	v_add_f32_e32 v86, s34, v88
	v_cmp_eq_u32_e64 s[22:23], v77, v82
	v_sub_co_u32_e32 v87, vcc, v82, v93
	s_nop 0
	v_cndmask_b32_e64 v77, v88, v86, s[22:23]
	v_add_u32_e32 v86, 0x110, v74
	v_lshl_add_u32 v87, v87, 2, s30
	v_cndmask_b32_e32 v231, v87, v86, vcc
	global_load_dwordx4 v[86:89], v[180:181], off offset:16
	global_load_dwordx4 v[126:129], v[180:181], off offset:128
	global_load_dwordx4 v[132:135], v[180:181], off offset:144
	ds_read_b32 v91, v230
	ds_read_b32 v94, v231
	v_or_b32_e32 v95, 5, v83
	v_sub_co_u32_e32 v97, vcc, v82, v95
	s_waitcnt lgkmcnt(1)
	v_add_f32_e32 v92, s34, v91
	v_add_u32_e32 v96, 0x114, v74
	v_lshl_add_u32 v97, v97, 2, s30
	v_cmp_eq_u32_e64 s[24:25], v90, v82
	v_cmp_eq_u32_e64 s[26:27], v93, v82
	v_or_b32_e32 v93, 6, v83
	v_cndmask_b32_e32 v233, v97, v96, vcc
	v_cndmask_b32_e64 v90, v91, v92, s[24:25]
	s_waitcnt lgkmcnt(0)
	v_add_f32_e32 v91, s34, v94
	v_cmp_eq_u32_e64 s[28:29], v95, v82
	v_sub_co_u32_e32 v95, vcc, v82, v93
	v_cndmask_b32_e64 v91, v94, v91, s[26:27]
	v_add_u32_e32 v94, 0x118, v74
	v_lshl_add_u32 v95, v95, 2, s30
	v_or_b32_e32 v83, 7, v83
	v_cndmask_b32_e32 v234, v95, v94, vcc
	v_sub_co_u32_e32 v95, vcc, v82, v83
	v_add_u32_e32 v74, 0x11c, v74
	v_lshl_add_u32 v95, v95, 2, s30
	ds_read_b32 v94, v234
	v_cndmask_b32_e32 v235, v95, v74, vcc
	ds_read_b32 v96, v233
	ds_read_b32 v74, v235
	v_cmp_eq_u32_e64 s[30:31], v93, v82
	s_waitcnt lgkmcnt(2)
	v_add_f32_e32 v95, s34, v94
	v_cvt_pk_f16_f32 v141, v77, v90
	s_waitcnt lgkmcnt(1)
	v_add_f32_e32 v92, s34, v96
	v_cndmask_b32_e64 v93, v94, v95, s[30:31]
	s_waitcnt lgkmcnt(0)
	v_add_f32_e32 v94, s34, v74
	v_cmp_eq_u32_e64 s[34:35], v83, v82
	v_cndmask_b32_e64 v92, v96, v92, s[28:29]
	v_cvt_pk_f16_f32 v142, v91, v92
	v_cndmask_b32_e64 v74, v74, v94, s[34:35]
	v_cvt_pk_f16_f32 v143, v93, v74
	v_cvt_pk_f16_f32 v140, v75, v76
	v_add_u32_e32 v232, v84, v85
	global_load_dwordx4 v[144:147], v[180:181], off offset:256
	global_load_dwordx4 v[148:151], v[180:181], off offset:272
	global_load_dwordx4 v[94:97], v[180:181], off offset:384
	global_load_dwordx4 v[118:121], v[180:181], off offset:400
	global_load_dwordx4 v[102:105], v[180:181], off offset:512
	global_load_dwordx4 v[114:117], v[180:181], off offset:528
	global_load_dwordx4 v[110:113], v[180:181], off offset:640
	global_load_dwordx4 v[106:109], v[180:181], off offset:656
	global_load_dwordx4 v[98:101], v[180:181], off offset:768
	global_load_dwordx4 v[90:93], v[180:181], off offset:784
	global_load_dwordx4 v[82:85], v[180:181], off offset:896
	global_load_dwordx4 v[74:77], v[180:181], off offset:912
	s_add_u32 s40, s40, s50
	s_addc_u32 s41, s41, s51
	s_add_u32 s42, s42, s50
	s_addc_u32 s43, s43, s51
	ds_write_b128 v232, v[140:143]
	s_waitcnt lgkmcnt(0)
	s_barrier
	s_waitcnt vmcnt(15)
	v_cvt_f32_f16_e32 v125, v79
	v_cvt_f32_f16_e32 v124, v78
	v_cvt_f32_f16_sdwa v79, v79 dst_sel:DWORD dst_unused:UNUSED_PAD src0_sel:WORD_1
	v_cvt_f32_f16_sdwa v78, v78 dst_sel:DWORD dst_unused:UNUSED_PAD src0_sel:WORD_1
	s_mov_b32 s52, s62
	v_pk_add_f32 v[124:125], v[124:125], 1.0 op_sel_hi:[1,0]
	s_mov_b32 s50, s64
	v_pk_fma_f32 v[70:71], v[70:71], v[124:125], v[78:79]
	v_cvt_f32_f16_e32 v79, v81
	v_cvt_f32_f16_e32 v78, v80
	v_cvt_f32_f16_sdwa v81, v81 dst_sel:DWORD dst_unused:UNUSED_PAD src0_sel:WORD_1
	v_cvt_f32_f16_sdwa v80, v80 dst_sel:DWORD dst_unused:UNUSED_PAD src0_sel:WORD_1
	s_waitcnt lgkmcnt(0)
	v_mov_b64_e32 v[124:125], s[52:53]
	v_pk_add_f32 v[78:79], v[78:79], 1.0 op_sel_hi:[1,0]
	v_pk_fma_f32 v[70:71], v[70:71], s[50:51], v[124:125] op_sel_hi:[1,0,0]
	v_pk_fma_f32 v[72:73], v[72:73], v[78:79], v[80:81]
	v_cvt_pk_f16_f32 v70, v70, v71
	v_pk_fma_f32 v[72:73], v[72:73], s[50:51], v[124:125] op_sel_hi:[1,0,0]
	v_or_b32_e32 v122, 0x80, v178
	v_cvt_pk_f16_f32 v71, v72, v73
	v_lshlrev_b32_e32 v240, 2, v189
	v_lshrrev_b32_e32 v131, 1, v188
	v_add_u32_e32 v190, 0, v238
	s_waitcnt vmcnt(14)
	v_cvt_f32_f16_e32 v79, v87
	v_cvt_f32_f16_e32 v78, v86
	v_cvt_f32_f16_sdwa v81, v87 dst_sel:DWORD dst_unused:UNUSED_PAD src0_sel:WORD_1
	v_cvt_f32_f16_sdwa v80, v86 dst_sel:DWORD dst_unused:UNUSED_PAD src0_sel:WORD_1
	v_pk_add_f32 v[72:73], v[78:79], 1.0 op_sel_hi:[1,0]
	v_cvt_f32_f16_e32 v79, v89
	v_cvt_f32_f16_e32 v78, v88
	v_pk_fma_f32 v[66:67], v[66:67], v[72:73], v[80:81]
	v_cvt_f32_f16_sdwa v81, v89 dst_sel:DWORD dst_unused:UNUSED_PAD src0_sel:WORD_1
	v_cvt_f32_f16_sdwa v80, v88 dst_sel:DWORD dst_unused:UNUSED_PAD src0_sel:WORD_1
	v_pk_fma_f32 v[66:67], v[66:67], s[50:51], v[124:125] op_sel_hi:[1,0,0]
	s_nop 0
	v_cvt_pk_f16_f32 v72, v66, v67
	v_pk_add_f32 v[66:67], v[78:79], 1.0 op_sel_hi:[1,0]
	s_waitcnt vmcnt(13)
	v_cvt_f32_f16_sdwa v79, v127 dst_sel:DWORD dst_unused:UNUSED_PAD src0_sel:WORD_1
	v_pk_fma_f32 v[66:67], v[68:69], v[66:67], v[80:81]
	v_cvt_f32_f16_e32 v69, v127
	v_cvt_f32_f16_e32 v68, v126
	v_cvt_f32_f16_sdwa v78, v126 dst_sel:DWORD dst_unused:UNUSED_PAD src0_sel:WORD_1
	v_pk_fma_f32 v[66:67], v[66:67], s[50:51], v[124:125] op_sel_hi:[1,0,0]
	s_nop 0
	v_cvt_pk_f16_f32 v73, v66, v67
	v_pk_add_f32 v[66:67], v[68:69], 1.0 op_sel_hi:[1,0]
	v_cvt_f32_f16_sdwa v69, v129 dst_sel:DWORD dst_unused:UNUSED_PAD src0_sel:WORD_1
	v_pk_fma_f32 v[62:63], v[62:63], v[66:67], v[78:79]
	v_cvt_f32_f16_e32 v67, v129
	v_cvt_f32_f16_e32 v66, v128
	v_cvt_f32_f16_sdwa v68, v128 dst_sel:DWORD dst_unused:UNUSED_PAD src0_sel:WORD_1
	v_pk_fma_f32 v[62:63], v[62:63], s[50:51], v[124:125] op_sel_hi:[1,0,0]
	s_nop 0
	v_cvt_pk_f16_f32 v78, v62, v63
	v_pk_add_f32 v[62:63], v[66:67], 1.0 op_sel_hi:[1,0]
	s_waitcnt vmcnt(12)
	v_cvt_f32_f16_sdwa v67, v133 dst_sel:DWORD dst_unused:UNUSED_PAD src0_sel:WORD_1
	v_pk_fma_f32 v[62:63], v[64:65], v[62:63], v[68:69]
	v_cvt_f32_f16_e32 v65, v133
	v_cvt_f32_f16_e32 v64, v132
	v_cvt_f32_f16_sdwa v66, v132 dst_sel:DWORD dst_unused:UNUSED_PAD src0_sel:WORD_1
	v_pk_fma_f32 v[62:63], v[62:63], s[50:51], v[124:125] op_sel_hi:[1,0,0]
	s_nop 0
	v_cvt_pk_f16_f32 v79, v62, v63
	v_pk_add_f32 v[62:63], v[64:65], 1.0 op_sel_hi:[1,0]
	v_cvt_f32_f16_sdwa v65, v135 dst_sel:DWORD dst_unused:UNUSED_PAD src0_sel:WORD_1
	v_pk_fma_f32 v[38:39], v[38:39], v[62:63], v[66:67]
	v_cvt_f32_f16_e32 v63, v135
	v_cvt_f32_f16_e32 v62, v134
	v_cvt_f32_f16_sdwa v64, v134 dst_sel:DWORD dst_unused:UNUSED_PAD src0_sel:WORD_1
	v_pk_fma_f32 v[38:39], v[38:39], s[50:51], v[124:125] op_sel_hi:[1,0,0]
	s_waitcnt vmcnt(4)
	v_cvt_f32_f16_sdwa v67, v107 dst_sel:DWORD dst_unused:UNUSED_PAD src0_sel:WORD_1
	v_cvt_pk_f16_f32 v80, v38, v39
	v_pk_add_f32 v[38:39], v[62:63], 1.0 op_sel_hi:[1,0]
	v_cvt_f32_f16_sdwa v63, v145 dst_sel:DWORD dst_unused:UNUSED_PAD src0_sel:WORD_1
	v_pk_fma_f32 v[38:39], v[40:41], v[38:39], v[64:65]
	v_cvt_f32_f16_e32 v41, v145
	v_cvt_f32_f16_e32 v40, v144
	v_cvt_f32_f16_sdwa v62, v144 dst_sel:DWORD dst_unused:UNUSED_PAD src0_sel:WORD_1
	v_pk_fma_f32 v[38:39], v[38:39], s[50:51], v[124:125] op_sel_hi:[1,0,0]
	v_cvt_f32_f16_e32 v65, v107
	v_cvt_pk_f16_f32 v81, v38, v39
	v_pk_add_f32 v[38:39], v[40:41], 1.0 op_sel_hi:[1,0]
	v_cvt_f32_f16_sdwa v41, v147 dst_sel:DWORD dst_unused:UNUSED_PAD src0_sel:WORD_1
	v_pk_fma_f32 v[34:35], v[34:35], v[38:39], v[62:63]
	v_cvt_f32_f16_e32 v39, v147
	v_cvt_f32_f16_e32 v38, v146
	v_cvt_f32_f16_sdwa v40, v146 dst_sel:DWORD dst_unused:UNUSED_PAD src0_sel:WORD_1
	v_pk_fma_f32 v[34:35], v[34:35], s[50:51], v[124:125] op_sel_hi:[1,0,0]
	v_cvt_f32_f16_e32 v64, v106
	v_cvt_pk_f16_f32 v86, v34, v35
	v_pk_add_f32 v[34:35], v[38:39], 1.0 op_sel_hi:[1,0]
	v_cvt_f32_f16_sdwa v39, v149 dst_sel:DWORD dst_unused:UNUSED_PAD src0_sel:WORD_1
	v_pk_fma_f32 v[34:35], v[36:37], v[34:35], v[40:41]
	v_cvt_f32_f16_e32 v37, v149
	v_cvt_f32_f16_e32 v36, v148
	v_cvt_f32_f16_sdwa v38, v148 dst_sel:DWORD dst_unused:UNUSED_PAD src0_sel:WORD_1
	v_pk_fma_f32 v[34:35], v[34:35], s[50:51], v[124:125] op_sel_hi:[1,0,0]
	v_cvt_f32_f16_sdwa v66, v106 dst_sel:DWORD dst_unused:UNUSED_PAD src0_sel:WORD_1
	v_cvt_pk_f16_f32 v87, v34, v35
	v_pk_add_f32 v[34:35], v[36:37], 1.0 op_sel_hi:[1,0]
	v_cvt_f32_f16_sdwa v37, v151 dst_sel:DWORD dst_unused:UNUSED_PAD src0_sel:WORD_1
	v_pk_fma_f32 v[30:31], v[30:31], v[34:35], v[38:39]
	v_cvt_f32_f16_e32 v35, v151
	v_cvt_f32_f16_e32 v34, v150
	v_cvt_f32_f16_sdwa v36, v150 dst_sel:DWORD dst_unused:UNUSED_PAD src0_sel:WORD_1
	v_pk_fma_f32 v[30:31], v[30:31], s[50:51], v[124:125] op_sel_hi:[1,0,0]
	s_nop 0
	v_cvt_pk_f16_f32 v88, v30, v31
	v_pk_add_f32 v[30:31], v[34:35], 1.0 op_sel_hi:[1,0]
	v_cvt_f32_f16_sdwa v35, v95 dst_sel:DWORD dst_unused:UNUSED_PAD src0_sel:WORD_1
	v_pk_fma_f32 v[30:31], v[32:33], v[30:31], v[36:37]
	v_cvt_f32_f16_e32 v33, v95
	v_cvt_f32_f16_e32 v32, v94
	v_cvt_f32_f16_sdwa v34, v94 dst_sel:DWORD dst_unused:UNUSED_PAD src0_sel:WORD_1
	v_pk_fma_f32 v[30:31], v[30:31], s[50:51], v[124:125] op_sel_hi:[1,0,0]
	s_nop 0
	v_cvt_pk_f16_f32 v89, v30, v31
	v_pk_add_f32 v[30:31], v[32:33], 1.0 op_sel_hi:[1,0]
	v_cvt_f32_f16_sdwa v33, v97 dst_sel:DWORD dst_unused:UNUSED_PAD src0_sel:WORD_1
	v_pk_fma_f32 v[26:27], v[26:27], v[30:31], v[34:35]
	v_cvt_f32_f16_e32 v31, v97
	v_cvt_f32_f16_e32 v30, v96
	v_cvt_f32_f16_sdwa v32, v96 dst_sel:DWORD dst_unused:UNUSED_PAD src0_sel:WORD_1
	v_pk_fma_f32 v[26:27], v[26:27], s[50:51], v[124:125] op_sel_hi:[1,0,0]
	s_nop 0
	v_cvt_pk_f16_f32 v94, v26, v27
	v_pk_add_f32 v[26:27], v[30:31], 1.0 op_sel_hi:[1,0]
	v_cvt_f32_f16_sdwa v31, v119 dst_sel:DWORD dst_unused:UNUSED_PAD src0_sel:WORD_1
	v_pk_fma_f32 v[26:27], v[28:29], v[26:27], v[32:33]
	v_cvt_f32_f16_e32 v29, v119
	v_cvt_f32_f16_e32 v28, v118
	v_cvt_f32_f16_sdwa v30, v118 dst_sel:DWORD dst_unused:UNUSED_PAD src0_sel:WORD_1
	v_pk_fma_f32 v[26:27], v[26:27], s[50:51], v[124:125] op_sel_hi:[1,0,0]
	s_nop 0
	v_cvt_pk_f16_f32 v95, v26, v27
	v_pk_add_f32 v[26:27], v[28:29], 1.0 op_sel_hi:[1,0]
	v_cvt_f32_f16_sdwa v29, v121 dst_sel:DWORD dst_unused:UNUSED_PAD src0_sel:WORD_1
	v_pk_fma_f32 v[22:23], v[22:23], v[26:27], v[30:31]
	v_cvt_f32_f16_e32 v27, v121
	v_cvt_f32_f16_e32 v26, v120
	v_cvt_f32_f16_sdwa v28, v120 dst_sel:DWORD dst_unused:UNUSED_PAD src0_sel:WORD_1
	v_pk_fma_f32 v[22:23], v[22:23], s[50:51], v[124:125] op_sel_hi:[1,0,0]
	s_nop 0
	v_cvt_pk_f16_f32 v96, v22, v23
	v_pk_add_f32 v[22:23], v[26:27], 1.0 op_sel_hi:[1,0]
	v_cvt_f32_f16_sdwa v27, v103 dst_sel:DWORD dst_unused:UNUSED_PAD src0_sel:WORD_1
	v_pk_fma_f32 v[22:23], v[24:25], v[22:23], v[28:29]
	v_cvt_f32_f16_e32 v25, v103
	v_cvt_f32_f16_e32 v24, v102
	v_cvt_f32_f16_sdwa v26, v102 dst_sel:DWORD dst_unused:UNUSED_PAD src0_sel:WORD_1
	v_pk_fma_f32 v[22:23], v[22:23], s[50:51], v[124:125] op_sel_hi:[1,0,0]
	s_nop 0
	v_cvt_pk_f16_f32 v97, v22, v23
	v_pk_add_f32 v[22:23], v[24:25], 1.0 op_sel_hi:[1,0]
	v_cvt_f32_f16_sdwa v25, v105 dst_sel:DWORD dst_unused:UNUSED_PAD src0_sel:WORD_1
	v_pk_fma_f32 v[18:19], v[18:19], v[22:23], v[26:27]
	v_cvt_f32_f16_e32 v23, v105
	v_cvt_f32_f16_e32 v22, v104
	v_cvt_f32_f16_sdwa v24, v104 dst_sel:DWORD dst_unused:UNUSED_PAD src0_sel:WORD_1
	v_pk_fma_f32 v[18:19], v[18:19], s[50:51], v[124:125] op_sel_hi:[1,0,0]
	s_nop 0
	v_cvt_pk_f16_f32 v102, v18, v19
	v_pk_add_f32 v[18:19], v[22:23], 1.0 op_sel_hi:[1,0]
	v_cvt_f32_f16_sdwa v23, v115 dst_sel:DWORD dst_unused:UNUSED_PAD src0_sel:WORD_1
	v_pk_fma_f32 v[18:19], v[20:21], v[18:19], v[24:25]
	v_cvt_f32_f16_e32 v21, v115
	v_cvt_f32_f16_e32 v20, v114
	v_cvt_f32_f16_sdwa v22, v114 dst_sel:DWORD dst_unused:UNUSED_PAD src0_sel:WORD_1
	v_pk_fma_f32 v[18:19], v[18:19], s[50:51], v[124:125] op_sel_hi:[1,0,0]
	s_nop 0
	v_cvt_pk_f16_f32 v103, v18, v19
	v_pk_add_f32 v[18:19], v[20:21], 1.0 op_sel_hi:[1,0]
	v_cvt_f32_f16_sdwa v21, v117 dst_sel:DWORD dst_unused:UNUSED_PAD src0_sel:WORD_1
	v_pk_fma_f32 v[14:15], v[14:15], v[18:19], v[22:23]
	v_cvt_f32_f16_e32 v19, v117
	v_cvt_f32_f16_e32 v18, v116
	v_cvt_f32_f16_sdwa v20, v116 dst_sel:DWORD dst_unused:UNUSED_PAD src0_sel:WORD_1
	v_pk_fma_f32 v[14:15], v[14:15], s[50:51], v[124:125] op_sel_hi:[1,0,0]
	s_nop 0
	v_cvt_pk_f16_f32 v104, v14, v15
	v_pk_add_f32 v[14:15], v[18:19], 1.0 op_sel_hi:[1,0]
	v_cvt_f32_f16_sdwa v19, v111 dst_sel:DWORD dst_unused:UNUSED_PAD src0_sel:WORD_1
	v_pk_fma_f32 v[14:15], v[16:17], v[14:15], v[20:21]
	v_cvt_f32_f16_e32 v17, v111
	v_cvt_f32_f16_e32 v16, v110
	v_cvt_f32_f16_sdwa v18, v110 dst_sel:DWORD dst_unused:UNUSED_PAD src0_sel:WORD_1
	v_pk_fma_f32 v[14:15], v[14:15], s[50:51], v[124:125] op_sel_hi:[1,0,0]
	s_nop 0
	v_cvt_pk_f16_f32 v105, v14, v15
	v_pk_add_f32 v[14:15], v[16:17], 1.0 op_sel_hi:[1,0]
	v_cvt_f32_f16_sdwa v17, v113 dst_sel:DWORD dst_unused:UNUSED_PAD src0_sel:WORD_1
	v_pk_fma_f32 v[10:11], v[10:11], v[14:15], v[18:19]
	v_cvt_f32_f16_e32 v15, v113
	v_cvt_f32_f16_e32 v14, v112
	v_cvt_f32_f16_sdwa v16, v112 dst_sel:DWORD dst_unused:UNUSED_PAD src0_sel:WORD_1
	v_pk_fma_f32 v[10:11], v[10:11], s[50:51], v[124:125] op_sel_hi:[1,0,0]
	s_nop 0
	v_cvt_pk_f16_f32 v110, v10, v11
	v_pk_add_f32 v[10:11], v[14:15], 1.0 op_sel_hi:[1,0]
	s_nop 0
	v_pk_fma_f32 v[62:63], v[12:13], v[10:11], v[16:17]
	v_lshl_add_u64 v[10:11], v[182:183], 0, v[178:179]
	global_load_dwordx4 v[34:37], v[10:11], off offset:16
	global_load_dwordx4 v[38:41], v[10:11], off
	v_lshl_add_u64 v[10:11], v[182:183], 0, v[122:123]
	v_or_b32_e32 v122, 0x100, v178
	global_load_dwordx4 v[26:29], v[10:11], off offset:16
	global_load_dwordx4 v[30:33], v[10:11], off
	v_lshl_add_u64 v[10:11], v[182:183], 0, v[122:123]
	v_or_b32_e32 v122, 0x180, v178
	v_lshl_add_u64 v[14:15], v[182:183], 0, v[122:123]
	global_load_dwordx4 v[18:21], v[10:11], off offset:16
	global_load_dwordx4 v[22:25], v[10:11], off
	s_nop 0
	global_load_dwordx4 v[10:13], v[14:15], off offset:16
	s_nop 0
	global_load_dwordx4 v[14:17], v[14:15], off
	v_pk_fma_f32 v[62:63], v[62:63], s[50:51], v[124:125] op_sel_hi:[1,0,0]
	s_nop 0
	v_cvt_pk_f16_f32 v111, v62, v63
	v_pk_add_f32 v[62:63], v[64:65], 1.0 op_sel_hi:[1,0]
	v_cvt_f32_f16_sdwa v65, v109 dst_sel:DWORD dst_unused:UNUSED_PAD src0_sel:WORD_1
	v_pk_fma_f32 v[58:59], v[58:59], v[62:63], v[66:67]
	v_cvt_f32_f16_e32 v63, v109
	v_cvt_f32_f16_e32 v62, v108
	v_cvt_f32_f16_sdwa v64, v108 dst_sel:DWORD dst_unused:UNUSED_PAD src0_sel:WORD_1
	v_pk_fma_f32 v[58:59], v[58:59], s[50:51], v[124:125] op_sel_hi:[1,0,0]
	s_nop 0
	v_cvt_pk_f16_f32 v112, v58, v59
	v_pk_add_f32 v[58:59], v[62:63], 1.0 op_sel_hi:[1,0]
	s_waitcnt vmcnt(11)
	v_cvt_f32_f16_sdwa v63, v99 dst_sel:DWORD dst_unused:UNUSED_PAD src0_sel:WORD_1
	v_pk_fma_f32 v[58:59], v[60:61], v[58:59], v[64:65]
	v_cvt_f32_f16_e32 v61, v99
	v_cvt_f32_f16_e32 v60, v98
	v_cvt_f32_f16_sdwa v62, v98 dst_sel:DWORD dst_unused:UNUSED_PAD src0_sel:WORD_1
	v_pk_fma_f32 v[58:59], v[58:59], s[50:51], v[124:125] op_sel_hi:[1,0,0]
	s_nop 0
	v_cvt_pk_f16_f32 v113, v58, v59
	v_pk_add_f32 v[58:59], v[60:61], 1.0 op_sel_hi:[1,0]
	v_cvt_f32_f16_sdwa v61, v101 dst_sel:DWORD dst_unused:UNUSED_PAD src0_sel:WORD_1
	v_pk_fma_f32 v[54:55], v[54:55], v[58:59], v[62:63]
	v_cvt_f32_f16_e32 v59, v101
	v_cvt_f32_f16_e32 v58, v100
	v_cvt_f32_f16_sdwa v60, v100 dst_sel:DWORD dst_unused:UNUSED_PAD src0_sel:WORD_1
	v_pk_fma_f32 v[54:55], v[54:55], s[50:51], v[124:125] op_sel_hi:[1,0,0]
	s_nop 0
	v_cvt_pk_f16_f32 v126, v54, v55
	v_pk_add_f32 v[54:55], v[58:59], 1.0 op_sel_hi:[1,0]
	s_waitcnt vmcnt(10)
	v_cvt_f32_f16_sdwa v59, v91 dst_sel:DWORD dst_unused:UNUSED_PAD src0_sel:WORD_1
	v_pk_fma_f32 v[54:55], v[56:57], v[54:55], v[60:61]
	v_cvt_f32_f16_e32 v57, v91
	v_cvt_f32_f16_e32 v56, v90
	v_cvt_f32_f16_sdwa v58, v90 dst_sel:DWORD dst_unused:UNUSED_PAD src0_sel:WORD_1
	v_pk_fma_f32 v[54:55], v[54:55], s[50:51], v[124:125] op_sel_hi:[1,0,0]
	s_nop 0
	v_cvt_pk_f16_f32 v127, v54, v55
	v_pk_add_f32 v[54:55], v[56:57], 1.0 op_sel_hi:[1,0]
	v_cvt_f32_f16_sdwa v57, v93 dst_sel:DWORD dst_unused:UNUSED_PAD src0_sel:WORD_1
	v_pk_fma_f32 v[50:51], v[50:51], v[54:55], v[58:59]
	v_cvt_f32_f16_e32 v55, v93
	v_cvt_f32_f16_e32 v54, v92
	v_cvt_f32_f16_sdwa v56, v92 dst_sel:DWORD dst_unused:UNUSED_PAD src0_sel:WORD_1
	v_pk_fma_f32 v[50:51], v[50:51], s[50:51], v[124:125] op_sel_hi:[1,0,0]
	s_nop 0
	v_cvt_pk_f16_f32 v128, v50, v51
	v_pk_add_f32 v[50:51], v[54:55], 1.0 op_sel_hi:[1,0]
	s_waitcnt vmcnt(9)
	v_cvt_f32_f16_sdwa v55, v83 dst_sel:DWORD dst_unused:UNUSED_PAD src0_sel:WORD_1
	v_pk_fma_f32 v[50:51], v[52:53], v[50:51], v[56:57]
	v_cvt_f32_f16_e32 v53, v83
	v_cvt_f32_f16_e32 v52, v82
	v_cvt_f32_f16_sdwa v54, v82 dst_sel:DWORD dst_unused:UNUSED_PAD src0_sel:WORD_1
	v_pk_fma_f32 v[50:51], v[50:51], s[50:51], v[124:125] op_sel_hi:[1,0,0]
	s_nop 0
	v_cvt_pk_f16_f32 v129, v50, v51
	v_pk_add_f32 v[50:51], v[52:53], 1.0 op_sel_hi:[1,0]
	v_cvt_f32_f16_sdwa v53, v85 dst_sel:DWORD dst_unused:UNUSED_PAD src0_sel:WORD_1
	v_pk_fma_f32 v[46:47], v[46:47], v[50:51], v[54:55]
	v_cvt_f32_f16_e32 v51, v85
	v_cvt_f32_f16_e32 v50, v84
	v_cvt_f32_f16_sdwa v52, v84 dst_sel:DWORD dst_unused:UNUSED_PAD src0_sel:WORD_1
	v_pk_fma_f32 v[46:47], v[46:47], s[50:51], v[124:125] op_sel_hi:[1,0,0]
	s_nop 0
	v_cvt_pk_f16_f32 v134, v46, v47
	v_pk_add_f32 v[46:47], v[50:51], 1.0 op_sel_hi:[1,0]
	s_waitcnt vmcnt(8)
	v_cvt_f32_f16_sdwa v51, v75 dst_sel:DWORD dst_unused:UNUSED_PAD src0_sel:WORD_1
	v_pk_fma_f32 v[46:47], v[48:49], v[46:47], v[52:53]
	v_cvt_f32_f16_e32 v49, v75
	v_cvt_f32_f16_e32 v48, v74
	v_cvt_f32_f16_sdwa v50, v74 dst_sel:DWORD dst_unused:UNUSED_PAD src0_sel:WORD_1
	v_pk_fma_f32 v[46:47], v[46:47], s[50:51], v[124:125] op_sel_hi:[1,0,0]
	s_nop 0
	v_cvt_pk_f16_f32 v135, v46, v47
	v_pk_add_f32 v[46:47], v[48:49], 1.0 op_sel_hi:[1,0]
	v_cvt_f32_f16_sdwa v49, v77 dst_sel:DWORD dst_unused:UNUSED_PAD src0_sel:WORD_1
	v_pk_fma_f32 v[42:43], v[42:43], v[46:47], v[50:51]
	v_cvt_f32_f16_e32 v47, v77
	v_cvt_f32_f16_e32 v46, v76
	v_cvt_f32_f16_sdwa v48, v76 dst_sel:DWORD dst_unused:UNUSED_PAD src0_sel:WORD_1
	v_pk_fma_f32 v[42:43], v[42:43], s[50:51], v[124:125] op_sel_hi:[1,0,0]
	s_nop 0
	v_cvt_pk_f16_f32 v136, v42, v43
	v_pk_add_f32 v[42:43], v[46:47], 1.0 op_sel_hi:[1,0]
	s_nop 0
	v_pk_fma_f32 v[42:43], v[44:45], v[42:43], v[48:49]
	s_nop 0
	v_pk_fma_f32 v[42:43], v[42:43], s[50:51], v[124:125] op_sel_hi:[1,0,0]
	s_nop 0
	v_cvt_pk_f16_f32 v137, v42, v43
	v_xor_b32_e32 v42, v189, v131
	v_lshlrev_b32_e32 v139, 4, v42
	v_add_u32_e32 v236, v130, v139
	ds_read_b128 v[42:45], v236
	ds_read_b128 v[46:49], v236 offset:2048
	v_bitop3_b32 v62, v189, v131, 4 bitop3:0x36
	v_lshlrev_b32_e32 v152, 4, v62
	v_add_u32_e32 v237, v130, v152
	s_waitcnt lgkmcnt(1)
	v_mfma_f32_16x16x32_f16 v[50:53], v[42:45], v[70:73], 0
	ds_read_b128 v[62:65], v237
	ds_read_b128 v[66:69], v237 offset:2048
	v_or_b32_e32 v194, v138, v139
	v_or_b32_e32 v195, v138, v152
	v_mfma_f32_16x16x32_f16 v[54:57], v[42:45], v[86:89], 0
	v_lshlrev_b32_e32 v179, 7, v189
	v_mov_b32_e32 v241, v179
	v_mov_b32_e32 v242, v195
	v_mfma_f32_16x16x32_f16 v[58:61], v[42:45], v[102:105], 0
	v_mov_b32_e32 v243, v194
	v_mfma_f32_16x16x32_f16 v[42:45], v[42:45], v[126:129], 0
	s_waitcnt lgkmcnt(1)
	v_mfma_f32_16x16x32_f16 v[130:133], v[62:65], v[78:81], v[50:53]
	v_mfma_f32_16x16x32_f16 v[122:125], v[62:65], v[94:97], v[54:57]
	v_mfma_f32_16x16x32_f16 v[114:117], v[62:65], v[134:137], v[42:45]
	v_mfma_f32_16x16x32_f16 v[42:45], v[46:49], v[70:73], 0
	v_mfma_f32_16x16x32_f16 v[50:53], v[46:49], v[86:89], 0
	v_mfma_f32_16x16x32_f16 v[54:57], v[46:49], v[102:105], 0
	v_mfma_f32_16x16x32_f16 v[46:49], v[46:49], v[126:129], 0
	s_waitcnt lgkmcnt(0)
	v_mfma_f32_16x16x32_f16 v[106:109], v[66:69], v[78:81], v[42:45]
	v_mfma_f32_16x16x32_f16 v[82:85], v[66:69], v[134:137], v[46:49]
	s_nop 1
	ds_read_b128 v[42:45], v236 offset:4096
	s_nop 1
	ds_read_b128 v[46:49], v236 offset:6144
	ds_read_b128 v[140:143], v237 offset:4096
	ds_read_b128 v[144:147], v237 offset:6144
	v_mfma_f32_16x16x32_f16 v[118:121], v[62:65], v[110:113], v[58:61]
	v_mfma_f32_16x16x32_f16 v[98:101], v[66:69], v[94:97], v[50:53]
	v_mfma_f32_16x16x32_f16 v[90:93], v[66:69], v[110:113], v[54:57]
	s_waitcnt lgkmcnt(3)
	v_mfma_f32_16x16x32_f16 v[50:53], v[42:45], v[70:73], 0
	v_mfma_f32_16x16x32_f16 v[54:57], v[42:45], v[86:89], 0
	v_mfma_f32_16x16x32_f16 v[58:61], v[42:45], v[102:105], 0
	v_mfma_f32_16x16x32_f16 v[42:45], v[42:45], v[126:129], 0
	s_waitcnt lgkmcnt(1)
	v_mfma_f32_16x16x32_f16 v[74:77], v[140:143], v[78:81], v[50:53]
	v_mfma_f32_16x16x32_f16 v[66:69], v[140:143], v[94:97], v[54:57]
	v_mfma_f32_16x16x32_f16 v[62:65], v[140:143], v[110:113], v[58:61]
	v_mfma_f32_16x16x32_f16 v[58:61], v[140:143], v[134:137], v[42:45]
	v_mfma_f32_16x16x32_f16 v[42:45], v[46:49], v[70:73], 0
	v_mfma_f32_16x16x32_f16 v[50:53], v[46:49], v[86:89], 0
	v_mfma_f32_16x16x32_f16 v[140:143], v[46:49], v[102:105], 0
	v_mfma_f32_16x16x32_f16 v[148:151], v[46:49], v[126:129], 0
	s_waitcnt lgkmcnt(0)
	v_mfma_f32_16x16x32_f16 v[54:57], v[144:147], v[78:81], v[42:45]
	v_mfma_f32_16x16x32_f16 v[50:53], v[144:147], v[94:97], v[50:53]
	v_mfma_f32_16x16x32_f16 v[46:49], v[144:147], v[110:113], v[140:143]
	v_mfma_f32_16x16x32_f16 v[42:45], v[144:147], v[134:137], v[148:151]

.LBB3_27:
	v_add_u32_e32 v142, 0, v176
	ds_read_b128 v[138:141], v142
	ds_read_b128 v[142:145], v142 offset:2048
	s_waitcnt lgkmcnt(1)
	v_mfma_f32_16x16x32_f16 v[146:149], v[138:141], v[70:73], 0
	v_mfma_f32_16x16x32_f16 v[150:153], v[138:141], v[86:89], 0
	v_mfma_f32_16x16x32_f16 v[154:157], v[138:141], v[102:105], 0
	v_mfma_f32_16x16x32_f16 v[158:161], v[138:141], v[126:129], 0
	v_add_u32_e32 v138, 0, v177
	ds_read_b128 v[162:165], v138
	ds_read_b128 v[166:169], v138 offset:2048
	s_waitcnt lgkmcnt(1)
	v_mfma_f32_16x16x32_f16 v[242:245], v[162:165], v[78:81], v[146:149]
	v_mfma_f32_16x16x32_f16 v[138:141], v[162:165], v[94:97], v[150:153]
	v_mfma_f32_16x16x32_f16 v[146:149], v[162:165], v[110:113], v[154:157]
	v_mfma_f32_16x16x32_f16 v[162:165], v[162:165], v[134:137], v[158:161]
	v_mfma_f32_16x16x32_f16 v[150:153], v[142:145], v[70:73], 0
	v_mfma_f32_16x16x32_f16 v[154:157], v[142:145], v[86:89], 0
	v_mfma_f32_16x16x32_f16 v[158:161], v[142:145], v[102:105], 0
	v_mfma_f32_16x16x32_f16 v[246:249], v[142:145], v[126:129], 0
	s_waitcnt lgkmcnt(0)
	v_mfma_f32_16x16x32_f16 v[170:173], v[166:169], v[78:81], v[150:153]
	v_mfma_f32_16x16x32_f16 v[142:145], v[166:169], v[94:97], v[154:157]
	v_mfma_f32_16x16x32_f16 v[154:157], v[166:169], v[110:113], v[158:161]
	v_mfma_f32_16x16x32_f16 v[158:161], v[166:169], v[134:137], v[246:249]
	v_add_u32_e32 v185, 0, v184
	v_add_u32_e32 v150, 0x12600, v185
	ds_read_b128 v[150:153], v150
	v_add_u32_e32 v166, 0x12620, v185
	ds_read_b64 v[186:187], v166
	v_add_u32_e32 v166, 0x12610, v185
	ds_read_b128 v[166:169], v166
	s_waitcnt lgkmcnt(2)
	v_fma_f32 v241, v150, v162, v146
	v_fma_f32 v241, -v151, v163, v241
	v_fma_f32 v246, v150, v163, v147
	v_fmac_f32_e32 v246, v151, v162
	v_fma_f32 v247, v150, v241, v138
	v_fma_f32 v247, -v151, v246, v247
	v_fma_f32 v246, v150, v246, v139
	v_fmac_f32_e32 v246, v151, v241
	v_fma_f32 v241, v150, v247, v242
	v_fma_f32 v241, -v151, v246, v241
	v_fma_f32 v250, v150, v246, v243
	v_fmac_f32_e32 v250, v151, v247
	v_mov_b32_dpp v242, v241 row_shl:1 row_mask:0xf bank_mask:0xf bound_ctrl:1
	v_fmac_f32_e32 v241, v152, v242
	v_mov_b32_dpp v243, v250 row_shl:1 row_mask:0xf bank_mask:0xf bound_ctrl:1
	v_fma_f32 v241, -v153, v243, v241
	v_fmac_f32_e32 v250, v152, v243
	v_fmac_f32_e32 v250, v153, v242
	v_mov_b32_dpp v152, v241 row_shl:2 row_mask:0xf bank_mask:0xf bound_ctrl:1
	v_add_u32_e32 v242, 0x12660, v185
	v_mov_b32_dpp v153, v250 row_shl:2 row_mask:0xf bank_mask:0xf bound_ctrl:1
	ds_read_b64 v[242:243], v242
	s_waitcnt lgkmcnt(1)
	v_fmac_f32_e32 v241, v166, v152
	v_fma_f32 v241, -v167, v153, v241
	v_fmac_f32_e32 v250, v166, v153
	v_fmac_f32_e32 v250, v167, v152
	v_mov_b32_dpp v152, v241 row_shl:4 row_mask:0xf bank_mask:0xf bound_ctrl:1
	v_fmac_f32_e32 v241, v168, v152
	v_mov_b32_dpp v153, v250 row_shl:4 row_mask:0xf bank_mask:0xf bound_ctrl:1
	v_fma_f32 v166, -v169, v153, v241
	v_fmac_f32_e32 v250, v168, v153
	v_fmac_f32_e32 v250, v169, v152
	v_mov_b32_dpp v152, v166 row_shl:8 row_mask:0xf bank_mask:0xf bound_ctrl:1
	v_fmac_f32_e32 v166, v186, v152
	v_mov_b32_dpp v153, v250 row_shl:8 row_mask:0xf bank_mask:0xf bound_ctrl:1
	v_fma_f32 v241, -v187, v153, v166
	v_add_u32_e32 v166, 0x12640, v185
	v_add_u32_e32 v167, 0x12650, v185
	ds_read_b128 v[246:249], v167
	ds_read_b128 v[166:169], v166
	v_fmac_f32_e32 v250, v186, v153
	v_fmac_f32_e32 v250, v187, v152
	v_mov_b32_dpp v152, v241 row_shl:1 row_mask:0xf bank_mask:0xf bound_ctrl:1
	s_waitcnt lgkmcnt(0)
	v_fma_f32 v186, v166, v164, v148
	v_fma_f32 v186, -v167, v165, v186
	v_fma_f32 v187, v166, v165, v149
	v_fmac_f32_e32 v187, v167, v164
	v_fma_f32 v241, v166, v186, v140
	v_fma_f32 v241, -v167, v187, v241
	v_fma_f32 v187, v166, v187, v141
	v_fmac_f32_e32 v187, v167, v186
	v_fma_f32 v186, v166, v241, v244
	v_fma_f32 v186, -v167, v187, v186
	v_fmac_f32_e32 v245, v166, v187
	v_fmac_f32_e32 v245, v167, v241
	v_mov_b32_dpp v187, v186 row_shl:1 row_mask:0xf bank_mask:0xf bound_ctrl:1
	v_fmac_f32_e32 v186, v168, v187
	v_mov_b32_dpp v241, v245 row_shl:1 row_mask:0xf bank_mask:0xf bound_ctrl:1
	v_fma_f32 v186, -v169, v241, v186
	v_fmac_f32_e32 v245, v168, v241
	v_fmac_f32_e32 v245, v169, v187
	v_mov_b32_dpp v168, v186 row_shl:2 row_mask:0xf bank_mask:0xf bound_ctrl:1
	v_fmac_f32_e32 v186, v246, v168
	v_mov_b32_dpp v169, v245 row_shl:2 row_mask:0xf bank_mask:0xf bound_ctrl:1
	v_fma_f32 v186, -v247, v169, v186
	v_fmac_f32_e32 v245, v246, v169
	v_fmac_f32_e32 v245, v247, v168
	v_mov_b32_dpp v168, v186 row_shl:4 row_mask:0xf bank_mask:0xf bound_ctrl:1
	v_fmac_f32_e32 v186, v248, v168
	v_mov_b32_dpp v169, v245 row_shl:4 row_mask:0xf bank_mask:0xf bound_ctrl:1
	v_fma_f32 v186, -v249, v169, v186
	v_fmac_f32_e32 v245, v248, v169
	v_fmac_f32_e32 v245, v249, v168
	v_mov_b32_dpp v168, v186 row_shl:8 row_mask:0xf bank_mask:0xf bound_ctrl:1
	v_fmac_f32_e32 v186, v242, v168
	v_mov_b32_dpp v169, v245 row_shl:8 row_mask:0xf bank_mask:0xf bound_ctrl:1
	v_fma_f32 v241, -v243, v169, v186
	v_fmac_f32_e32 v245, v242, v169
	v_add_u32_e32 v169, 0x12820, v185
	v_fmac_f32_e32 v245, v243, v168
	v_add_u32_e32 v168, 0x12800, v185
	ds_read_b64 v[186:187], v169
	ds_read_b128 v[246:249], v168
	v_mov_b32_dpp v168, v241 row_shl:1 row_mask:0xf bank_mask:0xf bound_ctrl:1
	v_add_u32_e32 v241, 0x12810, v185
	v_mov_b32_dpp v169, v245 row_shl:1 row_mask:0xf bank_mask:0xf bound_ctrl:1
	ds_read_b128 v[242:245], v241
	s_waitcnt lgkmcnt(1)
	v_fma_f32 v241, v246, v158, v154
	v_mov_b32_dpp v153, v250 row_shl:1 row_mask:0xf bank_mask:0xf bound_ctrl:1
	v_fma_f32 v241, -v247, v159, v241
	v_fma_f32 v250, v246, v159, v155
	v_fmac_f32_e32 v250, v247, v158
	v_fma_f32 v251, v246, v241, v142
	v_fma_f32 v251, -v247, v250, v251
	v_fma_f32 v250, v246, v250, v143
	v_fmac_f32_e32 v250, v247, v241
	v_fma_f32 v170, v246, v251, v170
	v_fma_f32 v170, -v247, v250, v170
	v_fma_f32 v241, v246, v250, v171
	v_fmac_f32_e32 v241, v247, v251
	v_mov_b32_dpp v171, v170 row_shl:1 row_mask:0xf bank_mask:0xf bound_ctrl:1
	v_fmac_f32_e32 v170, v248, v171
	v_mov_b32_dpp v250, v241 row_shl:1 row_mask:0xf bank_mask:0xf bound_ctrl:1
	v_fma_f32 v251, -v249, v250, v170
	v_fmac_f32_e32 v241, v248, v250
	v_fmac_f32_e32 v241, v249, v171
	v_mov_b32_dpp v248, v251 row_shl:2 row_mask:0xf bank_mask:0xf bound_ctrl:1
	s_waitcnt lgkmcnt(0)
	v_fmac_f32_e32 v251, v242, v248
	v_mov_b32_dpp v249, v241 row_shl:2 row_mask:0xf bank_mask:0xf bound_ctrl:1
	v_fma_f32 v250, -v243, v249, v251
	v_fmac_f32_e32 v241, v242, v249
	v_fmac_f32_e32 v241, v243, v248
	v_mov_b32_dpp v242, v250 row_shl:4 row_mask:0xf bank_mask:0xf bound_ctrl:1
	v_fmac_f32_e32 v250, v244, v242
	v_mov_b32_dpp v243, v241 row_shl:4 row_mask:0xf bank_mask:0xf bound_ctrl:1
	v_fma_f32 v248, -v245, v243, v250
	v_fmac_f32_e32 v241, v244, v243
	v_fmac_f32_e32 v241, v245, v242
	v_mov_b32_dpp v252, v248 row_shl:8 row_mask:0xf bank_mask:0xf bound_ctrl:1
	v_fmac_f32_e32 v248, v186, v252
	v_mov_b32_dpp v253, v241 row_shl:8 row_mask:0xf bank_mask:0xf bound_ctrl:1
	v_add_u32_e32 v170, 0x12860, v185
	v_fma_f32 v254, -v187, v253, v248
	v_add_u32_e32 v248, 0x12840, v185
	v_add_u32_e32 v185, 0x12850, v185
	ds_read_b64 v[170:171], v170
	ds_read_b128 v[242:245], v185
	ds_read_b128 v[248:251], v248
	v_fmac_f32_e32 v241, v186, v253
	v_fmac_f32_e32 v241, v187, v252
	v_mov_b32_dpp v186, v254 row_shl:1 row_mask:0xf bank_mask:0xf bound_ctrl:1
	s_waitcnt lgkmcnt(0)
	v_fma_f32 v185, v248, v160, v156
	v_mov_b32_dpp v187, v241 row_shl:1 row_mask:0xf bank_mask:0xf bound_ctrl:1
	v_fma_f32 v185, -v249, v161, v185
	v_fma_f32 v241, v248, v161, v157
	v_fmac_f32_e32 v241, v249, v160
	v_fma_f32 v252, v248, v185, v144
	v_fma_f32 v252, -v249, v241, v252
	v_fma_f32 v241, v248, v241, v145
	v_fmac_f32_e32 v241, v249, v185
	v_fma_f32 v172, v248, v252, v172
	v_fmac_f32_e32 v173, v248, v241
	v_fma_f32 v172, -v249, v241, v172
	v_fmac_f32_e32 v173, v249, v252
	s_nop 0
	v_mov_b32_dpp v185, v172 row_shl:1 row_mask:0xf bank_mask:0xf bound_ctrl:1
	v_mov_b32_dpp v241, v173 row_shl:1 row_mask:0xf bank_mask:0xf bound_ctrl:1
	v_fmac_f32_e32 v172, v250, v185
	v_fmac_f32_e32 v173, v250, v241
	v_fma_f32 v172, -v251, v241, v172
	v_fmac_f32_e32 v173, v251, v185
	s_nop 0
	v_mov_b32_dpp v185, v172 row_shl:2 row_mask:0xf bank_mask:0xf bound_ctrl:1
	v_mov_b32_dpp v241, v173 row_shl:2 row_mask:0xf bank_mask:0xf bound_ctrl:1
	v_fmac_f32_e32 v172, v242, v185
	v_fmac_f32_e32 v173, v242, v241
	v_fma_f32 v172, -v243, v241, v172
	v_fmac_f32_e32 v173, v243, v185
	s_nop 0
	v_mov_b32_dpp v185, v172 row_shl:4 row_mask:0xf bank_mask:0xf bound_ctrl:1
	v_mov_b32_dpp v241, v173 row_shl:4 row_mask:0xf bank_mask:0xf bound_ctrl:1
	v_fmac_f32_e32 v172, v244, v185
	v_fmac_f32_e32 v173, v244, v241
	v_fma_f32 v172, -v245, v241, v172
	v_fmac_f32_e32 v173, v245, v185
	s_nop 0
	v_mov_b32_dpp v185, v172 row_shl:8 row_mask:0xf bank_mask:0xf bound_ctrl:1
	v_mov_b32_dpp v241, v173 row_shl:8 row_mask:0xf bank_mask:0xf bound_ctrl:1
	v_fmac_f32_e32 v172, v170, v185
	v_fmac_f32_e32 v173, v170, v241
	v_fma_f32 v172, -v171, v241, v172
	v_fmac_f32_e32 v173, v171, v185
	s_nop 0
	v_mov_b32_dpp v170, v172 row_shl:1 row_mask:0xf bank_mask:0xf bound_ctrl:1
	v_mov_b32_dpp v171, v173 row_shl:1 row_mask:0xf bank_mask:0xf bound_ctrl:1
	v_pk_fma_f32 v[172:173], v[150:151], v[152:153], v[162:163] op_sel_hi:[0,1,1]
	v_pk_fma_f32 v[158:159], v[246:247], v[186:187], v[158:159] op_sel_hi:[0,1,1]
	v_pk_fma_f32 v[160:161], v[248:249], v[170:171], v[160:161] op_sel_hi:[0,1,1]
	v_add_u32_e32 v163, s33, v189
	v_cvt_pk_f16_f32 v162, v152, v153
	v_pk_fma_f32 v[164:165], v[166:167], v[168:169], v[164:165] op_sel_hi:[0,1,1]
	v_pk_fma_f32 v[152:153], v[150:151], v[152:153], v[172:173] op_sel:[1,1,0] op_sel_hi:[1,0,1] neg_lo:[1,0,0]
	v_pk_fma_f32 v[172:173], v[246:247], v[186:187], v[158:159] op_sel:[1,1,0] op_sel_hi:[1,0,1] neg_lo:[1,0,0]
	v_pk_fma_f32 v[160:161], v[248:249], v[170:171], v[160:161] op_sel:[1,1,0] op_sel_hi:[1,0,1] neg_lo:[1,0,0]
	v_xor_b32_e32 v163, v163, v188
	v_pk_fma_f32 v[164:165], v[166:167], v[168:169], v[164:165] op_sel:[1,1,0] op_sel_hi:[1,0,1] neg_lo:[1,0,0]
	v_pk_fma_f32 v[158:159], v[150:151], v[152:153], v[146:147] op_sel_hi:[0,1,1]
	v_pk_fma_f32 v[154:155], v[246:247], v[172:173], v[154:155] op_sel_hi:[0,1,1]
	v_pk_fma_f32 v[156:157], v[248:249], v[160:161], v[156:157] op_sel_hi:[0,1,1]
	v_lshl_add_u32 v185, v163, 4, v190
	v_cvt_pk_f16_f32 v146, v152, v153
	v_pk_fma_f32 v[148:149], v[166:167], v[164:165], v[148:149] op_sel_hi:[0,1,1]
	v_pk_fma_f32 v[242:243], v[150:151], v[152:153], v[158:159] op_sel:[1,1,0] op_sel_hi:[1,0,1] neg_lo:[1,0,0]
	v_pk_fma_f32 v[244:245], v[246:247], v[172:173], v[154:155] op_sel:[1,1,0] op_sel_hi:[1,0,1] neg_lo:[1,0,0]
	v_pk_fma_f32 v[250:251], v[248:249], v[160:161], v[156:157] op_sel:[1,1,0] op_sel_hi:[1,0,1] neg_lo:[1,0,0]
	ds_read_b128 v[152:155], v185 offset:49152
	ds_read_b128 v[156:159], v185 offset:53248
	v_pk_fma_f32 v[148:149], v[166:167], v[164:165], v[148:149] op_sel:[1,1,0] op_sel_hi:[1,0,1] neg_lo:[1,0,0]
	v_pk_fma_f32 v[252:253], v[150:151], v[242:243], v[138:139] op_sel_hi:[0,1,1]
	v_pk_fma_f32 v[142:143], v[246:247], v[244:245], v[142:143] op_sel_hi:[0,1,1]
	v_pk_fma_f32 v[140:141], v[166:167], v[148:149], v[140:141] op_sel_hi:[0,1,1]
	v_pk_fma_f32 v[144:145], v[248:249], v[250:251], v[144:145] op_sel_hi:[0,1,1]
	v_cvt_pk_f16_f32 v138, v242, v243
	v_pk_fma_f32 v[150:151], v[150:151], v[242:243], v[252:253] op_sel:[1,1,0] op_sel_hi:[1,0,1] neg_lo:[1,0,0]
	v_pk_fma_f32 v[242:243], v[246:247], v[244:245], v[142:143] op_sel:[1,1,0] op_sel_hi:[1,0,1] neg_lo:[1,0,0]
	v_pk_fma_f32 v[140:141], v[166:167], v[148:149], v[140:141] op_sel:[1,1,0] op_sel_hi:[1,0,1] neg_lo:[1,0,0]
	v_pk_fma_f32 v[166:167], v[248:249], v[250:251], v[144:145] op_sel:[1,1,0] op_sel_hi:[1,0,1] neg_lo:[1,0,0]
	v_cvt_pk_f16_f32 v142, v150, v151
	v_cvt_pk_f16_f32 v144, v242, v243
	v_cvt_pk_f16_f32 v143, v140, v141
	v_cvt_pk_f16_f32 v145, v166, v167
	v_cvt_pk_f16_f32 v140, v244, v245
	v_cvt_pk_f16_f32 v139, v148, v149
	v_cvt_pk_f16_f32 v141, v250, v251
	v_cvt_pk_f16_f32 v148, v172, v173
	v_cvt_pk_f16_f32 v147, v164, v165
	v_cvt_pk_f16_f32 v149, v160, v161
	v_cvt_pk_f16_f32 v164, v186, v187
	v_cvt_pk_f16_f32 v163, v168, v169
	v_cvt_pk_f16_f32 v165, v170, v171
	s_waitcnt lgkmcnt(1)
	v_mfma_f32_16x16x32_f16 v[130:133], v[152:155], v[142:145], v[130:133]
	s_add_i32 s33, s33, 4
	v_add_u32_e32 v184, 0x400, v184
	v_add_u32_e32 v177, 0x1000, v177
	v_mfma_f32_16x16x32_f16 v[122:125], v[152:155], v[138:141], v[122:125]
	s_cmp_lg_u32 s33, 16
	v_add_u32_e32 v176, 0x1000, v176
	v_mfma_f32_16x16x32_f16 v[118:121], v[152:155], v[146:149], v[118:121]
	v_mfma_f32_16x16x32_f16 v[114:117], v[152:155], v[162:165], v[114:117]
	s_waitcnt lgkmcnt(0)
	v_mfma_f32_16x16x32_f16 v[106:109], v[156:159], v[142:145], v[106:109]
	v_mfma_f32_16x16x32_f16 v[98:101], v[156:159], v[138:141], v[98:101]
	v_mfma_f32_16x16x32_f16 v[90:93], v[156:159], v[146:149], v[90:93]
	v_mfma_f32_16x16x32_f16 v[82:85], v[156:159], v[162:165], v[82:85]
	ds_read_b128 v[150:153], v185 offset:57344
	ds_read_b128 v[154:157], v185 offset:61440
	s_waitcnt lgkmcnt(1)
	v_mfma_f32_16x16x32_f16 v[74:77], v[150:153], v[142:145], v[74:77]
	v_mfma_f32_16x16x32_f16 v[66:69], v[150:153], v[138:141], v[66:69]
	v_mfma_f32_16x16x32_f16 v[62:65], v[150:153], v[146:149], v[62:65]
	v_mfma_f32_16x16x32_f16 v[58:61], v[150:153], v[162:165], v[58:61]
	s_waitcnt lgkmcnt(0)
	v_mfma_f32_16x16x32_f16 v[54:57], v[154:157], v[142:145], v[54:57]
	v_mfma_f32_16x16x32_f16 v[50:53], v[154:157], v[138:141], v[50:53]
	v_mfma_f32_16x16x32_f16 v[46:49], v[154:157], v[146:149], v[46:49]
	v_mfma_f32_16x16x32_f16 v[42:45], v[154:157], v[162:165], v[42:45]
	s_cbranch_scc1 .LBB3_27
	s_mov_b64 s[0:1], s[68:69]
	v_lshlrev_b32_e32 v136, 22, v239
	v_mov_b32_e32 v137, 0
	s_waitcnt lgkmcnt(0)
	v_lshl_add_u64 v[70:71], s[0:1], 0, v[136:137]
	v_lshlrev_b32_e32 v136, 1, v240
	v_lshl_add_u64 v[138:139], v[70:71], 0, v[136:137]
	v_mov_b32_e32 v176, v178
	v_mov_b32_e32 v177, 0
	v_lshl_add_u64 v[176:177], v[182:183], 0, v[176:177]
	global_load_dwordx4 v[148:151], v[176:177], off offset:528
	global_load_dwordx4 v[152:155], v[176:177], off offset:512
	global_load_dwordx4 v[156:159], v[176:177], off offset:656
	global_load_dwordx4 v[160:163], v[176:177], off offset:640
	global_load_dwordx4 v[164:167], v[176:177], off offset:784
	global_load_dwordx4 v[168:171], v[176:177], off offset:768
	global_load_dwordx4 v[184:187], v[176:177], off offset:912
	global_load_dwordx4 v[240:243], v[176:177], off offset:896
	s_lshl_b64 s[0:1], s[48:49], 13
	v_lshl_add_u64 v[72:73], v[138:139], 0, s[0:1]
	s_mov_b32 s1, 0x3f3504f3
	v_mul_f32_e64 v70, |v130|, s1
	s_mov_b32 s33, 0x3ea7ba05
	v_fma_f32 v71, v70, s33, 1.0
	v_rcp_f32_e32 v78, v71
	v_mul_f32_e32 v71, 0xbfb8aa3b, v70
	v_mul_f32_e32 v70, v70, v71
	v_exp_f32_e32 v80, v70
	v_mul_f32_e64 v70, |v131|, s1
	v_fma_f32 v71, v70, s33, 1.0
	v_rcp_f32_e32 v79, v71
	v_mul_f32_e32 v71, 0xbfb8aa3b, v70
	v_mul_f32_e32 v70, v70, v71
	s_mov_b32 s48, 0xbfba00e3
	v_exp_f32_e32 v81, v70
	s_mov_b32 s0, 0x3f87dc22
	v_mov_b64_e32 v[70:71], s[48:49]
	v_pk_fma_f32 v[86:87], v[78:79], s[0:1], v[70:71] op_sel_hi:[1,0,0]
	s_mov_b32 s48, 0x3fb5f0e3
	v_pk_fma_f32 v[86:87], v[78:79], v[86:87], s[48:49] op_sel_hi:[1,1,0]
	s_mov_b32 s50, 0xbe91a98e
	v_pk_fma_f32 v[86:87], v[78:79], v[86:87], s[50:51] op_sel_hi:[1,1,0]
	s_mov_b32 s52, 0x3e827906
	v_pk_fma_f32 v[86:87], v[78:79], v[86:87], s[52:53] op_sel_hi:[1,1,0]
	v_cmp_le_f32_e32 vcc, 0, v131
	v_pk_mul_f32 v[78:79], v[78:79], v[86:87]
	v_lshlrev_b32_e32 v136, 1, v238
	v_pk_mul_f32 v[78:79], v[78:79], 0.5 op_sel_hi:[1,0]
	v_lshl_add_u64 v[72:73], v[72:73], 0, v[136:137]
	v_pk_mul_f32 v[78:79], v[80:81], v[78:79]
	s_nop 0
	v_pk_mul_f32 v[80:81], v[130:131], v[78:79]
	v_pk_fma_f32 v[78:79], v[130:131], v[78:79], v[130:131] neg_lo:[1,0,0] neg_hi:[1,0,0]
	s_nop 0
	v_cndmask_b32_e32 v79, v81, v79, vcc
	v_cmp_le_f32_e32 vcc, 0, v130
	s_nop 1
	v_cndmask_b32_e32 v78, v80, v78, vcc
	v_cvt_pk_f16_f32 v78, v78, v79
	v_mul_f32_e64 v79, |v132|, s1
	v_mul_f32_e32 v81, 0xbfb8aa3b, v79
	v_fma_f32 v80, v79, s33, 1.0
	v_mul_f32_e32 v79, v79, v81
	v_exp_f32_e32 v86, v79
	v_mul_f32_e64 v79, |v133|, s1
	v_fma_f32 v81, v79, s33, 1.0
	v_rcp_f32_e32 v80, v80
	v_rcp_f32_e32 v81, v81
	v_mul_f32_e32 v87, 0xbfb8aa3b, v79
	v_mul_f32_e32 v79, v79, v87
	v_exp_f32_e32 v87, v79
	v_pk_fma_f32 v[88:89], v[80:81], s[0:1], v[70:71] op_sel_hi:[1,0,0]
	v_cmp_le_f32_e32 vcc, 0, v133
	v_pk_fma_f32 v[88:89], v[80:81], v[88:89], s[48:49] op_sel_hi:[1,1,0]
	s_nop 0
	v_pk_fma_f32 v[88:89], v[80:81], v[88:89], s[50:51] op_sel_hi:[1,1,0]
	s_nop 0
	v_pk_fma_f32 v[88:89], v[80:81], v[88:89], s[52:53] op_sel_hi:[1,1,0]
	s_nop 0
	v_pk_mul_f32 v[80:81], v[80:81], v[88:89]
	s_nop 0
	v_pk_mul_f32 v[80:81], v[80:81], 0.5 op_sel_hi:[1,0]
	s_nop 0
	v_pk_mul_f32 v[80:81], v[86:87], v[80:81]
	s_nop 0
	v_pk_mul_f32 v[86:87], v[132:133], v[80:81]
	v_pk_fma_f32 v[80:81], v[132:133], v[80:81], v[132:133] neg_lo:[1,0,0] neg_hi:[1,0,0]
	s_nop 0
	v_cndmask_b32_e32 v79, v87, v81, vcc
	v_cmp_le_f32_e32 vcc, 0, v132
	v_mul_f32_e64 v81, |v123|, s1
	s_nop 0
	v_cndmask_b32_e32 v80, v86, v80, vcc
	v_cvt_pk_f16_f32 v79, v80, v79
	global_store_dwordx2 v[72:73], v[78:79], off
	v_mul_f32_e64 v79, |v122|, s1
	v_mul_f32_e32 v80, 0xbfb8aa3b, v79
	v_fma_f32 v78, v79, s33, 1.0
	v_mul_f32_e32 v79, v79, v80
	v_exp_f32_e32 v80, v79
	v_fma_f32 v79, v81, s33, 1.0
	v_rcp_f32_e32 v78, v78
	v_rcp_f32_e32 v79, v79
	v_mul_f32_e32 v86, 0xbfb8aa3b, v81
	v_mul_f32_e32 v81, v81, v86
	v_exp_f32_e32 v81, v81
	v_pk_fma_f32 v[86:87], v[78:79], s[0:1], v[70:71] op_sel_hi:[1,0,0]
	v_cmp_le_f32_e32 vcc, 0, v123
	v_pk_fma_f32 v[86:87], v[78:79], v[86:87], s[48:49] op_sel_hi:[1,1,0]
	s_nop 0
	v_pk_fma_f32 v[86:87], v[78:79], v[86:87], s[50:51] op_sel_hi:[1,1,0]
	s_nop 0
	v_pk_fma_f32 v[86:87], v[78:79], v[86:87], s[52:53] op_sel_hi:[1,1,0]
	s_nop 0
	v_pk_mul_f32 v[78:79], v[78:79], v[86:87]
	s_nop 0
	v_pk_mul_f32 v[78:79], v[78:79], 0.5 op_sel_hi:[1,0]
	s_nop 0
	v_pk_mul_f32 v[78:79], v[80:81], v[78:79]
	s_nop 0
	v_pk_mul_f32 v[80:81], v[122:123], v[78:79]
	v_pk_fma_f32 v[78:79], v[122:123], v[78:79], v[122:123] neg_lo:[1,0,0] neg_hi:[1,0,0]
	s_nop 0
	v_cndmask_b32_e32 v79, v81, v79, vcc
	v_cmp_le_f32_e32 vcc, 0, v122
	s_nop 1
	v_cndmask_b32_e32 v78, v80, v78, vcc
	v_cvt_pk_f16_f32 v78, v78, v79
	v_mul_f32_e64 v79, |v124|, s1
	v_mul_f32_e32 v81, 0xbfb8aa3b, v79
	v_fma_f32 v80, v79, s33, 1.0
	v_mul_f32_e32 v79, v79, v81
	v_exp_f32_e32 v86, v79
	v_mul_f32_e64 v79, |v125|, s1
	v_fma_f32 v81, v79, s33, 1.0
	v_rcp_f32_e32 v80, v80
	v_rcp_f32_e32 v81, v81
	v_mul_f32_e32 v87, 0xbfb8aa3b, v79
	v_mul_f32_e32 v79, v79, v87
	v_exp_f32_e32 v87, v79
	v_pk_fma_f32 v[88:89], v[80:81], s[0:1], v[70:71] op_sel_hi:[1,0,0]
	v_cmp_le_f32_e32 vcc, 0, v125
	v_pk_fma_f32 v[88:89], v[80:81], v[88:89], s[48:49] op_sel_hi:[1,1,0]
	s_nop 0
	v_pk_fma_f32 v[88:89], v[80:81], v[88:89], s[50:51] op_sel_hi:[1,1,0]
	s_nop 0
	v_pk_fma_f32 v[88:89], v[80:81], v[88:89], s[52:53] op_sel_hi:[1,1,0]
	s_nop 0
	v_pk_mul_f32 v[80:81], v[80:81], v[88:89]
	s_nop 0
	v_pk_mul_f32 v[80:81], v[80:81], 0.5 op_sel_hi:[1,0]
	s_nop 0
	v_pk_mul_f32 v[80:81], v[86:87], v[80:81]
	s_nop 0
	v_pk_mul_f32 v[86:87], v[124:125], v[80:81]
	v_pk_fma_f32 v[80:81], v[124:125], v[80:81], v[124:125] neg_lo:[1,0,0] neg_hi:[1,0,0]
	s_nop 0
	v_cndmask_b32_e32 v79, v87, v81, vcc
	v_cmp_le_f32_e32 vcc, 0, v124
	v_mul_f32_e64 v81, |v119|, s1
	s_nop 0
	v_cndmask_b32_e32 v80, v86, v80, vcc
	v_cvt_pk_f16_f32 v79, v80, v79
	global_store_dwordx2 v[72:73], v[78:79], off offset:128
	v_mul_f32_e64 v79, |v118|, s1
	v_mul_f32_e32 v80, 0xbfb8aa3b, v79
	v_fma_f32 v78, v79, s33, 1.0
	v_mul_f32_e32 v79, v79, v80
	v_exp_f32_e32 v80, v79
	v_fma_f32 v79, v81, s33, 1.0
	v_rcp_f32_e32 v78, v78
	v_rcp_f32_e32 v79, v79
	v_mul_f32_e32 v86, 0xbfb8aa3b, v81
	v_mul_f32_e32 v81, v81, v86
	v_exp_f32_e32 v81, v81
	v_pk_fma_f32 v[86:87], v[78:79], s[0:1], v[70:71] op_sel_hi:[1,0,0]
	v_cmp_le_f32_e32 vcc, 0, v119
	v_pk_fma_f32 v[86:87], v[78:79], v[86:87], s[48:49] op_sel_hi:[1,1,0]
	s_nop 0
	v_pk_fma_f32 v[86:87], v[78:79], v[86:87], s[50:51] op_sel_hi:[1,1,0]
	s_nop 0
	v_pk_fma_f32 v[86:87], v[78:79], v[86:87], s[52:53] op_sel_hi:[1,1,0]
	s_nop 0
	v_pk_mul_f32 v[78:79], v[78:79], v[86:87]
	s_nop 0
	v_pk_mul_f32 v[78:79], v[78:79], 0.5 op_sel_hi:[1,0]
	s_nop 0
	v_pk_mul_f32 v[78:79], v[80:81], v[78:79]
	s_nop 0
	v_pk_mul_f32 v[80:81], v[118:119], v[78:79]
	v_pk_fma_f32 v[78:79], v[118:119], v[78:79], v[118:119] neg_lo:[1,0,0] neg_hi:[1,0,0]
	s_nop 0
	v_cndmask_b32_e32 v79, v81, v79, vcc
	v_cmp_le_f32_e32 vcc, 0, v118
	s_nop 1
	v_cndmask_b32_e32 v78, v80, v78, vcc
	v_cvt_pk_f16_f32 v78, v78, v79
	v_mul_f32_e64 v79, |v120|, s1
	v_mul_f32_e32 v81, 0xbfb8aa3b, v79
	v_fma_f32 v80, v79, s33, 1.0
	v_mul_f32_e32 v79, v79, v81
	v_exp_f32_e32 v86, v79
	v_mul_f32_e64 v79, |v121|, s1
	v_fma_f32 v81, v79, s33, 1.0
	v_rcp_f32_e32 v80, v80
	v_rcp_f32_e32 v81, v81
	v_mul_f32_e32 v87, 0xbfb8aa3b, v79
	v_mul_f32_e32 v79, v79, v87
	v_exp_f32_e32 v87, v79
	v_pk_fma_f32 v[88:89], v[80:81], s[0:1], v[70:71] op_sel_hi:[1,0,0]
	v_cmp_le_f32_e32 vcc, 0, v121
	v_pk_fma_f32 v[88:89], v[80:81], v[88:89], s[48:49] op_sel_hi:[1,1,0]
	s_nop 0
	v_pk_fma_f32 v[88:89], v[80:81], v[88:89], s[50:51] op_sel_hi:[1,1,0]
	s_nop 0
	v_pk_fma_f32 v[88:89], v[80:81], v[88:89], s[52:53] op_sel_hi:[1,1,0]
	s_nop 0
	v_pk_mul_f32 v[80:81], v[80:81], v[88:89]
	s_nop 0
	v_pk_mul_f32 v[80:81], v[80:81], 0.5 op_sel_hi:[1,0]
	s_nop 0
	v_pk_mul_f32 v[80:81], v[86:87], v[80:81]
	s_nop 0
	v_pk_mul_f32 v[86:87], v[120:121], v[80:81]
	v_pk_fma_f32 v[80:81], v[120:121], v[80:81], v[120:121] neg_lo:[1,0,0] neg_hi:[1,0,0]
	s_nop 0
	v_cndmask_b32_e32 v79, v87, v81, vcc
	v_cmp_le_f32_e32 vcc, 0, v120
	v_mul_f32_e64 v81, |v115|, s1
	s_nop 0
	v_cndmask_b32_e32 v80, v86, v80, vcc
	v_cvt_pk_f16_f32 v79, v80, v79
	global_store_dwordx2 v[72:73], v[78:79], off offset:256
	v_mul_f32_e64 v79, |v114|, s1
	v_mul_f32_e32 v80, 0xbfb8aa3b, v79
	v_fma_f32 v78, v79, s33, 1.0
	v_mul_f32_e32 v79, v79, v80
	v_exp_f32_e32 v80, v79
	v_fma_f32 v79, v81, s33, 1.0
	v_rcp_f32_e32 v78, v78
	v_rcp_f32_e32 v79, v79
	v_mul_f32_e32 v86, 0xbfb8aa3b, v81
	v_mul_f32_e32 v81, v81, v86
	v_exp_f32_e32 v81, v81
	v_pk_fma_f32 v[86:87], v[78:79], s[0:1], v[70:71] op_sel_hi:[1,0,0]
	v_cmp_le_f32_e32 vcc, 0, v115
	v_pk_fma_f32 v[86:87], v[78:79], v[86:87], s[48:49] op_sel_hi:[1,1,0]
	s_nop 0
	v_pk_fma_f32 v[86:87], v[78:79], v[86:87], s[50:51] op_sel_hi:[1,1,0]
	s_nop 0
	v_pk_fma_f32 v[86:87], v[78:79], v[86:87], s[52:53] op_sel_hi:[1,1,0]
	s_nop 0
	v_pk_mul_f32 v[78:79], v[78:79], v[86:87]
	s_nop 0
	v_pk_mul_f32 v[78:79], v[78:79], 0.5 op_sel_hi:[1,0]
	s_nop 0
	v_pk_mul_f32 v[78:79], v[80:81], v[78:79]
	s_nop 0
	v_pk_mul_f32 v[80:81], v[114:115], v[78:79]
	v_pk_fma_f32 v[78:79], v[114:115], v[78:79], v[114:115] neg_lo:[1,0,0] neg_hi:[1,0,0]
	s_nop 0
	v_cndmask_b32_e32 v79, v81, v79, vcc
	v_cmp_le_f32_e32 vcc, 0, v114
	s_nop 1
	v_cndmask_b32_e32 v78, v80, v78, vcc
	v_cvt_pk_f16_f32 v78, v78, v79
	v_mul_f32_e64 v79, |v116|, s1
	v_mul_f32_e32 v81, 0xbfb8aa3b, v79
	v_fma_f32 v80, v79, s33, 1.0
	v_mul_f32_e32 v79, v79, v81
	v_exp_f32_e32 v86, v79
	v_mul_f32_e64 v79, |v117|, s1
	v_fma_f32 v81, v79, s33, 1.0
	v_rcp_f32_e32 v80, v80
	v_rcp_f32_e32 v81, v81
	v_mul_f32_e32 v87, 0xbfb8aa3b, v79
	v_mul_f32_e32 v79, v79, v87
	v_exp_f32_e32 v87, v79
	v_pk_fma_f32 v[88:89], v[80:81], s[0:1], v[70:71] op_sel_hi:[1,0,0]
	v_cmp_le_f32_e32 vcc, 0, v117
	v_pk_fma_f32 v[88:89], v[80:81], v[88:89], s[48:49] op_sel_hi:[1,1,0]
	s_nop 0
	v_pk_fma_f32 v[88:89], v[80:81], v[88:89], s[50:51] op_sel_hi:[1,1,0]
	s_nop 0
	v_pk_fma_f32 v[88:89], v[80:81], v[88:89], s[52:53] op_sel_hi:[1,1,0]
	s_nop 0
	v_pk_mul_f32 v[80:81], v[80:81], v[88:89]
	s_nop 0
	v_pk_mul_f32 v[80:81], v[80:81], 0.5 op_sel_hi:[1,0]
	s_nop 0
	v_pk_mul_f32 v[80:81], v[86:87], v[80:81]
	s_nop 0
	v_pk_mul_f32 v[86:87], v[116:117], v[80:81]
	v_pk_fma_f32 v[80:81], v[116:117], v[80:81], v[116:117] neg_lo:[1,0,0] neg_hi:[1,0,0]
	s_nop 0
	v_cndmask_b32_e32 v79, v87, v81, vcc
	v_cmp_le_f32_e32 vcc, 0, v116
	v_mul_f32_e64 v81, |v107|, s1
	s_nop 0
	v_cndmask_b32_e32 v80, v86, v80, vcc
	v_cvt_pk_f16_f32 v79, v80, v79
	global_store_dwordx2 v[72:73], v[78:79], off offset:384
	v_mul_f32_e64 v79, |v106|, s1
	v_mul_f32_e32 v80, 0xbfb8aa3b, v79
	v_fma_f32 v78, v79, s33, 1.0
	v_mul_f32_e32 v79, v79, v80
	v_exp_f32_e32 v80, v79
	v_fma_f32 v79, v81, s33, 1.0
	v_rcp_f32_e32 v78, v78
	v_rcp_f32_e32 v79, v79
	v_mul_f32_e32 v86, 0xbfb8aa3b, v81
	v_mul_f32_e32 v81, v81, v86
	v_exp_f32_e32 v81, v81
	v_pk_fma_f32 v[86:87], v[78:79], s[0:1], v[70:71] op_sel_hi:[1,0,0]
	v_cmp_le_f32_e32 vcc, 0, v107
	v_pk_fma_f32 v[86:87], v[78:79], v[86:87], s[48:49] op_sel_hi:[1,1,0]
	s_nop 0
	v_pk_fma_f32 v[86:87], v[78:79], v[86:87], s[50:51] op_sel_hi:[1,1,0]
	s_nop 0
	v_pk_fma_f32 v[86:87], v[78:79], v[86:87], s[52:53] op_sel_hi:[1,1,0]
	s_nop 0
	v_pk_mul_f32 v[78:79], v[78:79], v[86:87]
	s_nop 0
	v_pk_mul_f32 v[78:79], v[78:79], 0.5 op_sel_hi:[1,0]
	s_nop 0
	v_pk_mul_f32 v[78:79], v[80:81], v[78:79]
	s_nop 0
	v_pk_mul_f32 v[80:81], v[106:107], v[78:79]
	v_pk_fma_f32 v[78:79], v[106:107], v[78:79], v[106:107] neg_lo:[1,0,0] neg_hi:[1,0,0]
	s_nop 0
	v_cndmask_b32_e32 v79, v81, v79, vcc
	v_cmp_le_f32_e32 vcc, 0, v106
	s_nop 1
	v_cndmask_b32_e32 v78, v80, v78, vcc
	v_cvt_pk_f16_f32 v78, v78, v79
	v_mul_f32_e64 v79, |v108|, s1
	v_mul_f32_e32 v81, 0xbfb8aa3b, v79
	v_fma_f32 v80, v79, s33, 1.0
	v_mul_f32_e32 v79, v79, v81
	v_exp_f32_e32 v86, v79
	v_mul_f32_e64 v79, |v109|, s1
	v_fma_f32 v81, v79, s33, 1.0
	v_rcp_f32_e32 v80, v80
	v_rcp_f32_e32 v81, v81
	v_mul_f32_e32 v87, 0xbfb8aa3b, v79
	v_mul_f32_e32 v79, v79, v87
	v_exp_f32_e32 v87, v79
	v_pk_fma_f32 v[88:89], v[80:81], s[0:1], v[70:71] op_sel_hi:[1,0,0]
	v_cmp_le_f32_e32 vcc, 0, v109
	v_pk_fma_f32 v[88:89], v[80:81], v[88:89], s[48:49] op_sel_hi:[1,1,0]
	s_nop 0
	v_pk_fma_f32 v[88:89], v[80:81], v[88:89], s[50:51] op_sel_hi:[1,1,0]
	s_nop 0
	v_pk_fma_f32 v[88:89], v[80:81], v[88:89], s[52:53] op_sel_hi:[1,1,0]
	s_nop 0
	v_pk_mul_f32 v[80:81], v[80:81], v[88:89]
	s_nop 0
	v_pk_mul_f32 v[80:81], v[80:81], 0.5 op_sel_hi:[1,0]
	s_nop 0
	v_pk_mul_f32 v[80:81], v[86:87], v[80:81]
	s_nop 0
	v_pk_mul_f32 v[86:87], v[108:109], v[80:81]
	v_pk_fma_f32 v[80:81], v[108:109], v[80:81], v[108:109] neg_lo:[1,0,0] neg_hi:[1,0,0]
	s_nop 0
	v_cndmask_b32_e32 v79, v87, v81, vcc
	v_cmp_le_f32_e32 vcc, 0, v108
	v_mul_f32_e64 v81, |v99|, s1
	s_nop 0
	v_cndmask_b32_e32 v80, v86, v80, vcc
	v_cvt_pk_f16_f32 v79, v80, v79
	global_store_dwordx2 v[72:73], v[78:79], off offset:32
	v_mul_f32_e64 v79, |v98|, s1
	v_mul_f32_e32 v80, 0xbfb8aa3b, v79
	v_fma_f32 v78, v79, s33, 1.0
	v_mul_f32_e32 v79, v79, v80
	v_exp_f32_e32 v80, v79
	v_fma_f32 v79, v81, s33, 1.0
	v_rcp_f32_e32 v78, v78
	v_rcp_f32_e32 v79, v79
	v_mul_f32_e32 v86, 0xbfb8aa3b, v81
	v_mul_f32_e32 v81, v81, v86
	v_exp_f32_e32 v81, v81
	v_pk_fma_f32 v[86:87], v[78:79], s[0:1], v[70:71] op_sel_hi:[1,0,0]
	v_cmp_le_f32_e32 vcc, 0, v99
	v_pk_fma_f32 v[86:87], v[78:79], v[86:87], s[48:49] op_sel_hi:[1,1,0]
	s_nop 0
	v_pk_fma_f32 v[86:87], v[78:79], v[86:87], s[50:51] op_sel_hi:[1,1,0]
	s_nop 0
	v_pk_fma_f32 v[86:87], v[78:79], v[86:87], s[52:53] op_sel_hi:[1,1,0]
	s_nop 0
	v_pk_mul_f32 v[78:79], v[78:79], v[86:87]
	s_nop 0
	v_pk_mul_f32 v[78:79], v[78:79], 0.5 op_sel_hi:[1,0]
	s_nop 0
	v_pk_mul_f32 v[78:79], v[80:81], v[78:79]
	s_nop 0
	v_pk_mul_f32 v[80:81], v[98:99], v[78:79]
	v_pk_fma_f32 v[78:79], v[98:99], v[78:79], v[98:99] neg_lo:[1,0,0] neg_hi:[1,0,0]
	s_nop 0
	v_cndmask_b32_e32 v79, v81, v79, vcc
	v_cmp_le_f32_e32 vcc, 0, v98
	s_nop 1
	v_cndmask_b32_e32 v78, v80, v78, vcc
	v_cvt_pk_f16_f32 v78, v78, v79
	v_mul_f32_e64 v79, |v100|, s1
	v_mul_f32_e32 v81, 0xbfb8aa3b, v79
	v_fma_f32 v80, v79, s33, 1.0
	v_mul_f32_e32 v79, v79, v81
	v_exp_f32_e32 v86, v79
	v_mul_f32_e64 v79, |v101|, s1
	v_fma_f32 v81, v79, s33, 1.0
	v_rcp_f32_e32 v80, v80
	v_rcp_f32_e32 v81, v81
	v_mul_f32_e32 v87, 0xbfb8aa3b, v79
	v_mul_f32_e32 v79, v79, v87
	v_exp_f32_e32 v87, v79
	v_pk_fma_f32 v[88:89], v[80:81], s[0:1], v[70:71] op_sel_hi:[1,0,0]
	v_cmp_le_f32_e32 vcc, 0, v101
	v_pk_fma_f32 v[88:89], v[80:81], v[88:89], s[48:49] op_sel_hi:[1,1,0]
	s_nop 0
	v_pk_fma_f32 v[88:89], v[80:81], v[88:89], s[50:51] op_sel_hi:[1,1,0]
	s_nop 0
	v_pk_fma_f32 v[88:89], v[80:81], v[88:89], s[52:53] op_sel_hi:[1,1,0]
	s_nop 0
	v_pk_mul_f32 v[80:81], v[80:81], v[88:89]
	s_nop 0
	v_pk_mul_f32 v[80:81], v[80:81], 0.5 op_sel_hi:[1,0]
	s_nop 0
	v_pk_mul_f32 v[80:81], v[86:87], v[80:81]
	s_nop 0
	v_pk_mul_f32 v[86:87], v[100:101], v[80:81]
	v_pk_fma_f32 v[80:81], v[100:101], v[80:81], v[100:101] neg_lo:[1,0,0] neg_hi:[1,0,0]
	s_nop 0
	v_cndmask_b32_e32 v79, v87, v81, vcc
	v_cmp_le_f32_e32 vcc, 0, v100
	v_mul_f32_e64 v81, |v91|, s1
	s_nop 0
	v_cndmask_b32_e32 v80, v86, v80, vcc
	v_cvt_pk_f16_f32 v79, v80, v79
	global_store_dwordx2 v[72:73], v[78:79], off offset:160
	v_mul_f32_e64 v79, |v90|, s1
	v_mul_f32_e32 v80, 0xbfb8aa3b, v79
	v_fma_f32 v78, v79, s33, 1.0
	v_mul_f32_e32 v79, v79, v80
	v_exp_f32_e32 v80, v79
	v_fma_f32 v79, v81, s33, 1.0
	v_rcp_f32_e32 v78, v78
	v_rcp_f32_e32 v79, v79
	v_mul_f32_e32 v86, 0xbfb8aa3b, v81
	v_mul_f32_e32 v81, v81, v86
	v_exp_f32_e32 v81, v81
	v_pk_fma_f32 v[86:87], v[78:79], s[0:1], v[70:71] op_sel_hi:[1,0,0]
	v_cmp_le_f32_e32 vcc, 0, v91
	v_pk_fma_f32 v[86:87], v[78:79], v[86:87], s[48:49] op_sel_hi:[1,1,0]
	s_nop 0
	v_pk_fma_f32 v[86:87], v[78:79], v[86:87], s[50:51] op_sel_hi:[1,1,0]
	s_nop 0
	v_pk_fma_f32 v[86:87], v[78:79], v[86:87], s[52:53] op_sel_hi:[1,1,0]
	s_nop 0
	v_pk_mul_f32 v[78:79], v[78:79], v[86:87]
	s_nop 0
	v_pk_mul_f32 v[78:79], v[78:79], 0.5 op_sel_hi:[1,0]
	s_nop 0
	v_pk_mul_f32 v[78:79], v[80:81], v[78:79]
	s_nop 0
	v_pk_mul_f32 v[80:81], v[90:91], v[78:79]
	v_pk_fma_f32 v[78:79], v[90:91], v[78:79], v[90:91] neg_lo:[1,0,0] neg_hi:[1,0,0]
	s_nop 0
	v_cndmask_b32_e32 v79, v81, v79, vcc
	v_cmp_le_f32_e32 vcc, 0, v90
	s_nop 1
	v_cndmask_b32_e32 v78, v80, v78, vcc
	v_cvt_pk_f16_f32 v78, v78, v79
	v_mul_f32_e64 v79, |v92|, s1
	v_mul_f32_e32 v81, 0xbfb8aa3b, v79
	v_fma_f32 v80, v79, s33, 1.0
	v_mul_f32_e32 v79, v79, v81
	v_exp_f32_e32 v86, v79
	v_mul_f32_e64 v79, |v93|, s1
	v_fma_f32 v81, v79, s33, 1.0
	v_rcp_f32_e32 v80, v80
	v_rcp_f32_e32 v81, v81
	v_mul_f32_e32 v87, 0xbfb8aa3b, v79
	v_mul_f32_e32 v79, v79, v87
	v_exp_f32_e32 v87, v79
	v_pk_fma_f32 v[88:89], v[80:81], s[0:1], v[70:71] op_sel_hi:[1,0,0]
	v_cmp_le_f32_e32 vcc, 0, v93
	v_pk_fma_f32 v[88:89], v[80:81], v[88:89], s[48:49] op_sel_hi:[1,1,0]
	s_nop 0
	v_pk_fma_f32 v[88:89], v[80:81], v[88:89], s[50:51] op_sel_hi:[1,1,0]
	s_nop 0
	v_pk_fma_f32 v[88:89], v[80:81], v[88:89], s[52:53] op_sel_hi:[1,1,0]
	s_nop 0
	v_pk_mul_f32 v[80:81], v[80:81], v[88:89]
	s_nop 0
	v_pk_mul_f32 v[80:81], v[80:81], 0.5 op_sel_hi:[1,0]
	s_nop 0
	v_pk_mul_f32 v[80:81], v[86:87], v[80:81]
	s_nop 0
	v_pk_mul_f32 v[86:87], v[92:93], v[80:81]
	v_pk_fma_f32 v[80:81], v[92:93], v[80:81], v[92:93] neg_lo:[1,0,0] neg_hi:[1,0,0]
	s_nop 0
	v_cndmask_b32_e32 v79, v87, v81, vcc
	v_cmp_le_f32_e32 vcc, 0, v92
	v_mul_f32_e64 v81, |v83|, s1
	s_nop 0
	v_cndmask_b32_e32 v80, v86, v80, vcc
	v_cvt_pk_f16_f32 v79, v80, v79
	global_store_dwordx2 v[72:73], v[78:79], off offset:288
	v_mul_f32_e64 v79, |v82|, s1
	v_mul_f32_e32 v80, 0xbfb8aa3b, v79
	v_fma_f32 v78, v79, s33, 1.0
	v_mul_f32_e32 v79, v79, v80
	v_exp_f32_e32 v80, v79
	v_fma_f32 v79, v81, s33, 1.0
	v_rcp_f32_e32 v78, v78
	v_rcp_f32_e32 v79, v79
	v_mul_f32_e32 v86, 0xbfb8aa3b, v81
	v_mul_f32_e32 v81, v81, v86
	v_exp_f32_e32 v81, v81
	v_pk_fma_f32 v[86:87], v[78:79], s[0:1], v[70:71] op_sel_hi:[1,0,0]
	v_cmp_le_f32_e32 vcc, 0, v83
	v_pk_fma_f32 v[86:87], v[78:79], v[86:87], s[48:49] op_sel_hi:[1,1,0]
	s_nop 0
	v_pk_fma_f32 v[86:87], v[78:79], v[86:87], s[50:51] op_sel_hi:[1,1,0]
	s_nop 0
	v_pk_fma_f32 v[86:87], v[78:79], v[86:87], s[52:53] op_sel_hi:[1,1,0]
	s_nop 0
	v_pk_mul_f32 v[78:79], v[78:79], v[86:87]
	s_nop 0
	v_pk_mul_f32 v[78:79], v[78:79], 0.5 op_sel_hi:[1,0]
	s_nop 0
	v_pk_mul_f32 v[78:79], v[80:81], v[78:79]
	s_nop 0
	v_pk_mul_f32 v[80:81], v[82:83], v[78:79]
	v_pk_fma_f32 v[78:79], v[82:83], v[78:79], v[82:83] neg_lo:[1,0,0] neg_hi:[1,0,0]
	s_nop 0
	v_cndmask_b32_e32 v79, v81, v79, vcc
	v_cmp_le_f32_e32 vcc, 0, v82
	s_nop 1
	v_cndmask_b32_e32 v78, v80, v78, vcc
	v_cvt_pk_f16_f32 v78, v78, v79
	v_mul_f32_e64 v79, |v84|, s1
	v_mul_f32_e32 v81, 0xbfb8aa3b, v79
	v_fma_f32 v80, v79, s33, 1.0
	v_mul_f32_e32 v79, v79, v81
	v_exp_f32_e32 v82, v79
	v_mul_f32_e64 v79, |v85|, s1
	v_fma_f32 v81, v79, s33, 1.0
	v_rcp_f32_e32 v80, v80
	v_rcp_f32_e32 v81, v81
	v_mul_f32_e32 v83, 0xbfb8aa3b, v79
	v_mul_f32_e32 v79, v79, v83
	v_exp_f32_e32 v83, v79
	v_pk_fma_f32 v[86:87], v[80:81], s[0:1], v[70:71] op_sel_hi:[1,0,0]
	v_cmp_le_f32_e32 vcc, 0, v85
	v_pk_fma_f32 v[86:87], v[80:81], v[86:87], s[48:49] op_sel_hi:[1,1,0]
	s_nop 0
	v_pk_fma_f32 v[86:87], v[80:81], v[86:87], s[50:51] op_sel_hi:[1,1,0]
	s_nop 0
	v_pk_fma_f32 v[86:87], v[80:81], v[86:87], s[52:53] op_sel_hi:[1,1,0]
	s_nop 0
	v_pk_mul_f32 v[80:81], v[80:81], v[86:87]
	s_nop 0
	v_pk_mul_f32 v[80:81], v[80:81], 0.5 op_sel_hi:[1,0]
	s_nop 0
	v_pk_mul_f32 v[80:81], v[82:83], v[80:81]
	s_nop 0
	v_pk_mul_f32 v[82:83], v[84:85], v[80:81]
	v_pk_fma_f32 v[80:81], v[84:85], v[80:81], v[84:85] neg_lo:[1,0,0] neg_hi:[1,0,0]
	s_nop 0
	v_cndmask_b32_e32 v79, v83, v81, vcc
	v_cmp_le_f32_e32 vcc, 0, v84
	v_mul_f32_e64 v81, |v75|, s1
	s_nop 0
	v_cndmask_b32_e32 v80, v82, v80, vcc
	v_cvt_pk_f16_f32 v79, v80, v79
	global_store_dwordx2 v[72:73], v[78:79], off offset:416
	v_mul_f32_e64 v79, |v74|, s1
	v_mul_f32_e32 v80, 0xbfb8aa3b, v79
	v_fma_f32 v78, v79, s33, 1.0
	v_mul_f32_e32 v79, v79, v80
	v_exp_f32_e32 v80, v79
	v_fma_f32 v79, v81, s33, 1.0
	v_rcp_f32_e32 v78, v78
	v_rcp_f32_e32 v79, v79
	v_mul_f32_e32 v82, 0xbfb8aa3b, v81
	v_mul_f32_e32 v81, v81, v82
	v_exp_f32_e32 v81, v81
	v_pk_fma_f32 v[82:83], v[78:79], s[0:1], v[70:71] op_sel_hi:[1,0,0]
	v_cmp_le_f32_e32 vcc, 0, v75
	v_pk_fma_f32 v[82:83], v[78:79], v[82:83], s[48:49] op_sel_hi:[1,1,0]
	s_nop 0
	v_pk_fma_f32 v[82:83], v[78:79], v[82:83], s[50:51] op_sel_hi:[1,1,0]
	s_nop 0
	v_pk_fma_f32 v[82:83], v[78:79], v[82:83], s[52:53] op_sel_hi:[1,1,0]
	s_nop 0
	v_pk_mul_f32 v[78:79], v[78:79], v[82:83]
	s_nop 0
	v_pk_mul_f32 v[78:79], v[78:79], 0.5 op_sel_hi:[1,0]
	s_nop 0
	v_pk_mul_f32 v[78:79], v[80:81], v[78:79]
	s_nop 0
	v_pk_mul_f32 v[80:81], v[74:75], v[78:79]
	v_pk_fma_f32 v[78:79], v[74:75], v[78:79], v[74:75] neg_lo:[1,0,0] neg_hi:[1,0,0]
	s_nop 0
	v_cndmask_b32_e32 v75, v81, v79, vcc
	v_cmp_le_f32_e32 vcc, 0, v74
	s_nop 1
	v_cndmask_b32_e32 v74, v80, v78, vcc
	v_cvt_pk_f16_f32 v74, v74, v75
	v_mul_f32_e64 v75, |v76|, s1
	v_mul_f32_e32 v79, 0xbfb8aa3b, v75
	v_fma_f32 v78, v75, s33, 1.0
	v_mul_f32_e32 v75, v75, v79
	v_exp_f32_e32 v80, v75
	v_mul_f32_e64 v75, |v77|, s1
	v_fma_f32 v79, v75, s33, 1.0
	v_rcp_f32_e32 v78, v78
	v_rcp_f32_e32 v79, v79
	v_mul_f32_e32 v81, 0xbfb8aa3b, v75
	v_mul_f32_e32 v75, v75, v81
	v_exp_f32_e32 v81, v75
	v_pk_fma_f32 v[82:83], v[78:79], s[0:1], v[70:71] op_sel_hi:[1,0,0]
	v_cmp_le_f32_e32 vcc, 0, v77
	v_pk_fma_f32 v[82:83], v[78:79], v[82:83], s[48:49] op_sel_hi:[1,1,0]
	s_nop 0
	v_pk_fma_f32 v[82:83], v[78:79], v[82:83], s[50:51] op_sel_hi:[1,1,0]
	s_nop 0
	v_pk_fma_f32 v[82:83], v[78:79], v[82:83], s[52:53] op_sel_hi:[1,1,0]
	s_nop 0
	v_pk_mul_f32 v[78:79], v[78:79], v[82:83]
	s_nop 0
	v_pk_mul_f32 v[78:79], v[78:79], 0.5 op_sel_hi:[1,0]
	s_nop 0
	v_pk_mul_f32 v[78:79], v[80:81], v[78:79]
	s_nop 0
	v_pk_mul_f32 v[80:81], v[76:77], v[78:79]
	v_pk_fma_f32 v[78:79], v[76:77], v[78:79], v[76:77] neg_lo:[1,0,0] neg_hi:[1,0,0]
	v_mul_f32_e64 v77, |v67|, s1
	v_cndmask_b32_e32 v75, v81, v79, vcc
	v_cmp_le_f32_e32 vcc, 0, v76
	s_nop 1
	v_cndmask_b32_e32 v76, v80, v78, vcc
	v_cvt_pk_f16_f32 v75, v76, v75
	global_store_dwordx2 v[72:73], v[74:75], off offset:64
	v_mul_f32_e64 v75, |v66|, s1
	v_mul_f32_e32 v76, 0xbfb8aa3b, v75
	v_fma_f32 v74, v75, s33, 1.0
	v_mul_f32_e32 v75, v75, v76
	v_exp_f32_e32 v76, v75
	v_fma_f32 v75, v77, s33, 1.0
	v_rcp_f32_e32 v74, v74
	v_rcp_f32_e32 v75, v75
	v_mul_f32_e32 v78, 0xbfb8aa3b, v77
	v_mul_f32_e32 v77, v77, v78
	v_exp_f32_e32 v77, v77
	v_pk_fma_f32 v[78:79], v[74:75], s[0:1], v[70:71] op_sel_hi:[1,0,0]
	v_cmp_le_f32_e32 vcc, 0, v67
	v_pk_fma_f32 v[78:79], v[74:75], v[78:79], s[48:49] op_sel_hi:[1,1,0]
	s_nop 0
	v_pk_fma_f32 v[78:79], v[74:75], v[78:79], s[50:51] op_sel_hi:[1,1,0]
	s_nop 0
	v_pk_fma_f32 v[78:79], v[74:75], v[78:79], s[52:53] op_sel_hi:[1,1,0]
	s_nop 0
	v_pk_mul_f32 v[74:75], v[74:75], v[78:79]
	s_nop 0
	v_pk_mul_f32 v[74:75], v[74:75], 0.5 op_sel_hi:[1,0]
	s_nop 0
	v_pk_mul_f32 v[74:75], v[76:77], v[74:75]
	s_nop 0
	v_pk_mul_f32 v[76:77], v[66:67], v[74:75]
	v_pk_fma_f32 v[74:75], v[66:67], v[74:75], v[66:67] neg_lo:[1,0,0] neg_hi:[1,0,0]
	s_nop 0
	v_cndmask_b32_e32 v67, v77, v75, vcc
	v_cmp_le_f32_e32 vcc, 0, v66
	s_nop 1
	v_cndmask_b32_e32 v66, v76, v74, vcc
	v_cvt_pk_f16_f32 v66, v66, v67
	v_mul_f32_e64 v67, |v68|, s1
	v_mul_f32_e32 v75, 0xbfb8aa3b, v67
	v_fma_f32 v74, v67, s33, 1.0
	v_mul_f32_e32 v67, v67, v75
	v_exp_f32_e32 v76, v67
	v_mul_f32_e64 v67, |v69|, s1
	v_fma_f32 v75, v67, s33, 1.0
	v_rcp_f32_e32 v74, v74
	v_rcp_f32_e32 v75, v75
	v_mul_f32_e32 v77, 0xbfb8aa3b, v67
	v_mul_f32_e32 v67, v67, v77
	v_exp_f32_e32 v77, v67
	v_pk_fma_f32 v[78:79], v[74:75], s[0:1], v[70:71] op_sel_hi:[1,0,0]
	v_cmp_le_f32_e32 vcc, 0, v69
	v_pk_fma_f32 v[78:79], v[74:75], v[78:79], s[48:49] op_sel_hi:[1,1,0]
	s_nop 0
	v_pk_fma_f32 v[78:79], v[74:75], v[78:79], s[50:51] op_sel_hi:[1,1,0]
	s_nop 0
	v_pk_fma_f32 v[78:79], v[74:75], v[78:79], s[52:53] op_sel_hi:[1,1,0]
	s_nop 0
	v_pk_mul_f32 v[74:75], v[74:75], v[78:79]
	s_nop 0
	v_pk_mul_f32 v[74:75], v[74:75], 0.5 op_sel_hi:[1,0]
	s_nop 0
	v_pk_mul_f32 v[74:75], v[76:77], v[74:75]
	s_nop 0
	v_pk_mul_f32 v[76:77], v[68:69], v[74:75]
	v_pk_fma_f32 v[74:75], v[68:69], v[74:75], v[68:69] neg_lo:[1,0,0] neg_hi:[1,0,0]
	v_mul_f32_e64 v69, |v63|, s1
	v_cndmask_b32_e32 v67, v77, v75, vcc
	v_cmp_le_f32_e32 vcc, 0, v68
	s_nop 1
	v_cndmask_b32_e32 v68, v76, v74, vcc
	v_cvt_pk_f16_f32 v67, v68, v67
	global_store_dwordx2 v[72:73], v[66:67], off offset:192
	v_mul_f32_e64 v67, |v62|, s1
	v_mul_f32_e32 v68, 0xbfb8aa3b, v67
	v_fma_f32 v66, v67, s33, 1.0
	v_mul_f32_e32 v67, v67, v68
	v_exp_f32_e32 v68, v67
	v_fma_f32 v67, v69, s33, 1.0
	v_rcp_f32_e32 v66, v66
	v_rcp_f32_e32 v67, v67
	v_mul_f32_e32 v74, 0xbfb8aa3b, v69
	v_mul_f32_e32 v69, v69, v74
	v_exp_f32_e32 v69, v69
	v_pk_fma_f32 v[74:75], v[66:67], s[0:1], v[70:71] op_sel_hi:[1,0,0]
	v_cmp_le_f32_e32 vcc, 0, v63
	v_pk_fma_f32 v[74:75], v[66:67], v[74:75], s[48:49] op_sel_hi:[1,1,0]
	s_nop 0
	v_pk_fma_f32 v[74:75], v[66:67], v[74:75], s[50:51] op_sel_hi:[1,1,0]
	s_nop 0
	v_pk_fma_f32 v[74:75], v[66:67], v[74:75], s[52:53] op_sel_hi:[1,1,0]
	s_nop 0
	v_pk_mul_f32 v[66:67], v[66:67], v[74:75]
	s_nop 0
	v_pk_mul_f32 v[66:67], v[66:67], 0.5 op_sel_hi:[1,0]
	s_nop 0
	v_pk_mul_f32 v[66:67], v[68:69], v[66:67]
	s_nop 0
	v_pk_mul_f32 v[68:69], v[62:63], v[66:67]
	v_pk_fma_f32 v[66:67], v[62:63], v[66:67], v[62:63] neg_lo:[1,0,0] neg_hi:[1,0,0]
	s_nop 0
	v_cndmask_b32_e32 v63, v69, v67, vcc
	v_cmp_le_f32_e32 vcc, 0, v62
	s_nop 1
	v_cndmask_b32_e32 v62, v68, v66, vcc
	v_cvt_pk_f16_f32 v62, v62, v63
	v_mul_f32_e64 v63, |v64|, s1
	v_mul_f32_e32 v67, 0xbfb8aa3b, v63
	v_fma_f32 v66, v63, s33, 1.0
	v_mul_f32_e32 v63, v63, v67
	v_exp_f32_e32 v68, v63
	v_mul_f32_e64 v63, |v65|, s1
	v_fma_f32 v67, v63, s33, 1.0
	v_rcp_f32_e32 v66, v66
	v_rcp_f32_e32 v67, v67
	v_mul_f32_e32 v69, 0xbfb8aa3b, v63
	v_mul_f32_e32 v63, v63, v69
	v_exp_f32_e32 v69, v63
	v_pk_fma_f32 v[74:75], v[66:67], s[0:1], v[70:71] op_sel_hi:[1,0,0]
	v_cmp_le_f32_e32 vcc, 0, v65
	v_pk_fma_f32 v[74:75], v[66:67], v[74:75], s[48:49] op_sel_hi:[1,1,0]
	s_nop 0
	v_pk_fma_f32 v[74:75], v[66:67], v[74:75], s[50:51] op_sel_hi:[1,1,0]
	s_nop 0
	v_pk_fma_f32 v[74:75], v[66:67], v[74:75], s[52:53] op_sel_hi:[1,1,0]
	s_nop 0
	v_pk_mul_f32 v[66:67], v[66:67], v[74:75]
	s_nop 0
	v_pk_mul_f32 v[66:67], v[66:67], 0.5 op_sel_hi:[1,0]
	s_nop 0
	v_pk_mul_f32 v[66:67], v[68:69], v[66:67]
	s_nop 0
	v_pk_mul_f32 v[68:69], v[64:65], v[66:67]
	v_pk_fma_f32 v[66:67], v[64:65], v[66:67], v[64:65] neg_lo:[1,0,0] neg_hi:[1,0,0]
	v_mul_f32_e64 v65, |v59|, s1
	v_cndmask_b32_e32 v63, v69, v67, vcc
	v_cmp_le_f32_e32 vcc, 0, v64
	s_nop 1
	v_cndmask_b32_e32 v64, v68, v66, vcc
	v_cvt_pk_f16_f32 v63, v64, v63
	global_store_dwordx2 v[72:73], v[62:63], off offset:320
	v_mul_f32_e64 v63, |v58|, s1
	v_mul_f32_e32 v64, 0xbfb8aa3b, v63
	v_fma_f32 v62, v63, s33, 1.0
	v_mul_f32_e32 v63, v63, v64
	v_exp_f32_e32 v64, v63
	v_fma_f32 v63, v65, s33, 1.0
	v_rcp_f32_e32 v62, v62
	v_rcp_f32_e32 v63, v63
	v_mul_f32_e32 v66, 0xbfb8aa3b, v65
	v_mul_f32_e32 v65, v65, v66
	v_exp_f32_e32 v65, v65
	v_pk_fma_f32 v[66:67], v[62:63], s[0:1], v[70:71] op_sel_hi:[1,0,0]
	v_cmp_le_f32_e32 vcc, 0, v59
	v_pk_fma_f32 v[66:67], v[62:63], v[66:67], s[48:49] op_sel_hi:[1,1,0]
	s_nop 0
	v_pk_fma_f32 v[66:67], v[62:63], v[66:67], s[50:51] op_sel_hi:[1,1,0]
	s_nop 0
	v_pk_fma_f32 v[66:67], v[62:63], v[66:67], s[52:53] op_sel_hi:[1,1,0]
	s_nop 0
	v_pk_mul_f32 v[62:63], v[62:63], v[66:67]
	s_nop 0
	v_pk_mul_f32 v[62:63], v[62:63], 0.5 op_sel_hi:[1,0]
	s_nop 0
	v_pk_mul_f32 v[62:63], v[64:65], v[62:63]
	s_nop 0
	v_pk_mul_f32 v[64:65], v[58:59], v[62:63]
	v_pk_fma_f32 v[62:63], v[58:59], v[62:63], v[58:59] neg_lo:[1,0,0] neg_hi:[1,0,0]
	s_nop 0
	v_cndmask_b32_e32 v59, v65, v63, vcc
	v_cmp_le_f32_e32 vcc, 0, v58
	s_nop 1
	v_cndmask_b32_e32 v58, v64, v62, vcc
	v_cvt_pk_f16_f32 v58, v58, v59
	v_mul_f32_e64 v59, |v60|, s1
	v_mul_f32_e32 v63, 0xbfb8aa3b, v59
	v_fma_f32 v62, v59, s33, 1.0
	v_mul_f32_e32 v59, v59, v63
	v_exp_f32_e32 v64, v59
	v_mul_f32_e64 v59, |v61|, s1
	v_fma_f32 v63, v59, s33, 1.0
	v_rcp_f32_e32 v62, v62
	v_rcp_f32_e32 v63, v63
	v_mul_f32_e32 v65, 0xbfb8aa3b, v59
	v_mul_f32_e32 v59, v59, v65
	v_exp_f32_e32 v65, v59
	v_pk_fma_f32 v[66:67], v[62:63], s[0:1], v[70:71] op_sel_hi:[1,0,0]
	v_cmp_le_f32_e32 vcc, 0, v61
	v_pk_fma_f32 v[66:67], v[62:63], v[66:67], s[48:49] op_sel_hi:[1,1,0]
	s_nop 0
	v_pk_fma_f32 v[66:67], v[62:63], v[66:67], s[50:51] op_sel_hi:[1,1,0]
	s_nop 0
	v_pk_fma_f32 v[66:67], v[62:63], v[66:67], s[52:53] op_sel_hi:[1,1,0]
	s_nop 0
	v_pk_mul_f32 v[62:63], v[62:63], v[66:67]
	s_nop 0
	v_pk_mul_f32 v[62:63], v[62:63], 0.5 op_sel_hi:[1,0]
	s_nop 0
	v_pk_mul_f32 v[62:63], v[64:65], v[62:63]
	s_nop 0
	v_pk_mul_f32 v[64:65], v[60:61], v[62:63]
	v_pk_fma_f32 v[62:63], v[60:61], v[62:63], v[60:61] neg_lo:[1,0,0] neg_hi:[1,0,0]
	v_mul_f32_e64 v61, |v55|, s1
	v_cndmask_b32_e32 v59, v65, v63, vcc
	v_cmp_le_f32_e32 vcc, 0, v60
	s_nop 1
	v_cndmask_b32_e32 v60, v64, v62, vcc
	v_cvt_pk_f16_f32 v59, v60, v59
	global_store_dwordx2 v[72:73], v[58:59], off offset:448
	v_mul_f32_e64 v59, |v54|, s1
	v_mul_f32_e32 v60, 0xbfb8aa3b, v59
	v_fma_f32 v58, v59, s33, 1.0
	v_mul_f32_e32 v59, v59, v60
	v_exp_f32_e32 v60, v59
	v_fma_f32 v59, v61, s33, 1.0
	v_rcp_f32_e32 v58, v58
	v_rcp_f32_e32 v59, v59
	v_mul_f32_e32 v62, 0xbfb8aa3b, v61
	v_mul_f32_e32 v61, v61, v62
	v_exp_f32_e32 v61, v61
	v_pk_fma_f32 v[62:63], v[58:59], s[0:1], v[70:71] op_sel_hi:[1,0,0]
	v_cmp_le_f32_e32 vcc, 0, v55
	v_pk_fma_f32 v[62:63], v[58:59], v[62:63], s[48:49] op_sel_hi:[1,1,0]
	s_nop 0
	v_pk_fma_f32 v[62:63], v[58:59], v[62:63], s[50:51] op_sel_hi:[1,1,0]
	s_nop 0
	v_pk_fma_f32 v[62:63], v[58:59], v[62:63], s[52:53] op_sel_hi:[1,1,0]
	s_nop 0
	v_pk_mul_f32 v[58:59], v[58:59], v[62:63]
	s_nop 0
	v_pk_mul_f32 v[58:59], v[58:59], 0.5 op_sel_hi:[1,0]
	s_nop 0
	v_pk_mul_f32 v[58:59], v[60:61], v[58:59]
	s_nop 0
	v_pk_mul_f32 v[60:61], v[54:55], v[58:59]
	v_pk_fma_f32 v[58:59], v[54:55], v[58:59], v[54:55] neg_lo:[1,0,0] neg_hi:[1,0,0]
	s_nop 0
	v_cndmask_b32_e32 v55, v61, v59, vcc
	v_cmp_le_f32_e32 vcc, 0, v54
	s_nop 1
	v_cndmask_b32_e32 v54, v60, v58, vcc
	v_cvt_pk_f16_f32 v54, v54, v55
	v_mul_f32_e64 v55, |v56|, s1
	v_mul_f32_e32 v59, 0xbfb8aa3b, v55
	v_fma_f32 v58, v55, s33, 1.0
	v_mul_f32_e32 v55, v55, v59
	v_exp_f32_e32 v60, v55
	v_mul_f32_e64 v55, |v57|, s1
	v_fma_f32 v59, v55, s33, 1.0
	v_rcp_f32_e32 v58, v58
	v_rcp_f32_e32 v59, v59
	v_mul_f32_e32 v61, 0xbfb8aa3b, v55
	v_mul_f32_e32 v55, v55, v61
	v_exp_f32_e32 v61, v55
	v_pk_fma_f32 v[62:63], v[58:59], s[0:1], v[70:71] op_sel_hi:[1,0,0]
	v_cmp_le_f32_e32 vcc, 0, v57
	v_pk_fma_f32 v[62:63], v[58:59], v[62:63], s[48:49] op_sel_hi:[1,1,0]
	s_nop 0
	v_pk_fma_f32 v[62:63], v[58:59], v[62:63], s[50:51] op_sel_hi:[1,1,0]
	s_nop 0
	v_pk_fma_f32 v[62:63], v[58:59], v[62:63], s[52:53] op_sel_hi:[1,1,0]
	s_nop 0
	v_pk_mul_f32 v[58:59], v[58:59], v[62:63]
	s_nop 0
	v_pk_mul_f32 v[58:59], v[58:59], 0.5 op_sel_hi:[1,0]
	s_nop 0
	v_pk_mul_f32 v[58:59], v[60:61], v[58:59]
	s_nop 0
	v_pk_mul_f32 v[60:61], v[56:57], v[58:59]
	v_pk_fma_f32 v[58:59], v[56:57], v[58:59], v[56:57] neg_lo:[1,0,0] neg_hi:[1,0,0]
	v_mul_f32_e64 v57, |v51|, s1
	v_cndmask_b32_e32 v55, v61, v59, vcc
	v_cmp_le_f32_e32 vcc, 0, v56
	s_nop 1
	v_cndmask_b32_e32 v56, v60, v58, vcc
	v_cvt_pk_f16_f32 v55, v56, v55
	global_store_dwordx2 v[72:73], v[54:55], off offset:96
	v_mul_f32_e64 v55, |v50|, s1
	v_mul_f32_e32 v56, 0xbfb8aa3b, v55
	v_fma_f32 v54, v55, s33, 1.0
	v_mul_f32_e32 v55, v55, v56
	v_exp_f32_e32 v56, v55
	v_fma_f32 v55, v57, s33, 1.0
	v_rcp_f32_e32 v54, v54
	v_rcp_f32_e32 v55, v55
	v_mul_f32_e32 v58, 0xbfb8aa3b, v57
	v_mul_f32_e32 v57, v57, v58
	v_exp_f32_e32 v57, v57
	v_pk_fma_f32 v[58:59], v[54:55], s[0:1], v[70:71] op_sel_hi:[1,0,0]
	v_cmp_le_f32_e32 vcc, 0, v51
	v_pk_fma_f32 v[58:59], v[54:55], v[58:59], s[48:49] op_sel_hi:[1,1,0]
	s_nop 0
	v_pk_fma_f32 v[58:59], v[54:55], v[58:59], s[50:51] op_sel_hi:[1,1,0]
	s_nop 0
	v_pk_fma_f32 v[58:59], v[54:55], v[58:59], s[52:53] op_sel_hi:[1,1,0]
	s_nop 0
	v_pk_mul_f32 v[54:55], v[54:55], v[58:59]
	s_nop 0
	v_pk_mul_f32 v[54:55], v[54:55], 0.5 op_sel_hi:[1,0]
	s_nop 0
	v_pk_mul_f32 v[54:55], v[56:57], v[54:55]
	s_nop 0
	v_pk_mul_f32 v[56:57], v[50:51], v[54:55]
	v_pk_fma_f32 v[54:55], v[50:51], v[54:55], v[50:51] neg_lo:[1,0,0] neg_hi:[1,0,0]
	s_nop 0
	v_cndmask_b32_e32 v51, v57, v55, vcc
	v_cmp_le_f32_e32 vcc, 0, v50
	s_nop 1
	v_cndmask_b32_e32 v50, v56, v54, vcc
	v_cvt_pk_f16_f32 v50, v50, v51
	v_mul_f32_e64 v51, |v52|, s1
	v_mul_f32_e32 v55, 0xbfb8aa3b, v51
	v_fma_f32 v54, v51, s33, 1.0
	v_mul_f32_e32 v51, v51, v55
	v_exp_f32_e32 v56, v51
	v_mul_f32_e64 v51, |v53|, s1
	v_fma_f32 v55, v51, s33, 1.0
	v_rcp_f32_e32 v54, v54
	v_rcp_f32_e32 v55, v55
	v_mul_f32_e32 v57, 0xbfb8aa3b, v51
	v_mul_f32_e32 v51, v51, v57
	v_exp_f32_e32 v57, v51
	v_pk_fma_f32 v[58:59], v[54:55], s[0:1], v[70:71] op_sel_hi:[1,0,0]
	v_cmp_le_f32_e32 vcc, 0, v53
	v_pk_fma_f32 v[58:59], v[54:55], v[58:59], s[48:49] op_sel_hi:[1,1,0]
	s_nop 0
	v_pk_fma_f32 v[58:59], v[54:55], v[58:59], s[50:51] op_sel_hi:[1,1,0]
	s_nop 0
	v_pk_fma_f32 v[58:59], v[54:55], v[58:59], s[52:53] op_sel_hi:[1,1,0]
	s_nop 0
	v_pk_mul_f32 v[54:55], v[54:55], v[58:59]
	s_nop 0
	v_pk_mul_f32 v[54:55], v[54:55], 0.5 op_sel_hi:[1,0]
	s_nop 0
	v_pk_mul_f32 v[54:55], v[56:57], v[54:55]
	s_nop 0
	v_pk_mul_f32 v[56:57], v[52:53], v[54:55]
	v_pk_fma_f32 v[54:55], v[52:53], v[54:55], v[52:53] neg_lo:[1,0,0] neg_hi:[1,0,0]
	v_mul_f32_e64 v53, |v47|, s1
	v_cndmask_b32_e32 v51, v57, v55, vcc
	v_cmp_le_f32_e32 vcc, 0, v52
	s_nop 1
	v_cndmask_b32_e32 v52, v56, v54, vcc
	v_cvt_pk_f16_f32 v51, v52, v51
	global_store_dwordx2 v[72:73], v[50:51], off offset:224
	v_mul_f32_e64 v51, |v46|, s1
	v_mul_f32_e32 v52, 0xbfb8aa3b, v51
	v_fma_f32 v50, v51, s33, 1.0
	v_mul_f32_e32 v51, v51, v52
	v_exp_f32_e32 v52, v51
	v_fma_f32 v51, v53, s33, 1.0
	v_rcp_f32_e32 v50, v50
	v_rcp_f32_e32 v51, v51
	v_mul_f32_e32 v54, 0xbfb8aa3b, v53
	v_mul_f32_e32 v53, v53, v54
	v_exp_f32_e32 v53, v53
	v_pk_fma_f32 v[54:55], v[50:51], s[0:1], v[70:71] op_sel_hi:[1,0,0]
	v_cmp_le_f32_e32 vcc, 0, v47
	v_pk_fma_f32 v[54:55], v[50:51], v[54:55], s[48:49] op_sel_hi:[1,1,0]
	s_nop 0
	v_pk_fma_f32 v[54:55], v[50:51], v[54:55], s[50:51] op_sel_hi:[1,1,0]
	s_nop 0
	v_pk_fma_f32 v[54:55], v[50:51], v[54:55], s[52:53] op_sel_hi:[1,1,0]
	s_nop 0
	v_pk_mul_f32 v[50:51], v[50:51], v[54:55]
	s_nop 0
	v_pk_mul_f32 v[50:51], v[50:51], 0.5 op_sel_hi:[1,0]
	s_nop 0
	v_pk_mul_f32 v[50:51], v[52:53], v[50:51]
	s_nop 0
	v_pk_mul_f32 v[52:53], v[46:47], v[50:51]
	v_pk_fma_f32 v[50:51], v[46:47], v[50:51], v[46:47] neg_lo:[1,0,0] neg_hi:[1,0,0]
	s_nop 0
	v_cndmask_b32_e32 v47, v53, v51, vcc
	v_cmp_le_f32_e32 vcc, 0, v46
	s_nop 1
	v_cndmask_b32_e32 v46, v52, v50, vcc
	v_cvt_pk_f16_f32 v46, v46, v47
	v_mul_f32_e64 v47, |v48|, s1
	v_mul_f32_e32 v51, 0xbfb8aa3b, v47
	v_fma_f32 v50, v47, s33, 1.0
	v_mul_f32_e32 v47, v47, v51
	v_exp_f32_e32 v52, v47
	v_mul_f32_e64 v47, |v49|, s1
	v_fma_f32 v51, v47, s33, 1.0
	v_rcp_f32_e32 v50, v50
	v_rcp_f32_e32 v51, v51
	v_mul_f32_e32 v53, 0xbfb8aa3b, v47
	v_mul_f32_e32 v47, v47, v53
	v_exp_f32_e32 v53, v47
	v_pk_fma_f32 v[54:55], v[50:51], s[0:1], v[70:71] op_sel_hi:[1,0,0]
	v_cmp_le_f32_e32 vcc, 0, v49
	v_pk_fma_f32 v[54:55], v[50:51], v[54:55], s[48:49] op_sel_hi:[1,1,0]
	s_nop 0
	v_pk_fma_f32 v[54:55], v[50:51], v[54:55], s[50:51] op_sel_hi:[1,1,0]
	s_nop 0
	v_pk_fma_f32 v[54:55], v[50:51], v[54:55], s[52:53] op_sel_hi:[1,1,0]
	s_nop 0
	v_pk_mul_f32 v[50:51], v[50:51], v[54:55]
	s_nop 0
	v_pk_mul_f32 v[50:51], v[50:51], 0.5 op_sel_hi:[1,0]
	s_nop 0
	v_pk_mul_f32 v[50:51], v[52:53], v[50:51]
	s_nop 0
	v_pk_mul_f32 v[52:53], v[48:49], v[50:51]
	v_pk_fma_f32 v[50:51], v[48:49], v[50:51], v[48:49] neg_lo:[1,0,0] neg_hi:[1,0,0]
	v_mul_f32_e64 v49, |v43|, s1
	v_cndmask_b32_e32 v47, v53, v51, vcc
	v_cmp_le_f32_e32 vcc, 0, v48
	s_nop 1
	v_cndmask_b32_e32 v48, v52, v50, vcc
	v_cvt_pk_f16_f32 v47, v48, v47
	global_store_dwordx2 v[72:73], v[46:47], off offset:352
	v_mul_f32_e64 v47, |v42|, s1
	v_mul_f32_e32 v48, 0xbfb8aa3b, v47
	v_fma_f32 v46, v47, s33, 1.0
	v_mul_f32_e32 v47, v47, v48
	v_exp_f32_e32 v48, v47
	v_fma_f32 v47, v49, s33, 1.0
	v_rcp_f32_e32 v46, v46
	v_rcp_f32_e32 v47, v47
	v_mul_f32_e32 v50, 0xbfb8aa3b, v49
	v_mul_f32_e32 v49, v49, v50
	v_exp_f32_e32 v49, v49
	v_pk_fma_f32 v[50:51], v[46:47], s[0:1], v[70:71] op_sel_hi:[1,0,0]
	v_cmp_le_f32_e32 vcc, 0, v43
	v_pk_fma_f32 v[50:51], v[46:47], v[50:51], s[48:49] op_sel_hi:[1,1,0]
	s_nop 0
	v_pk_fma_f32 v[50:51], v[46:47], v[50:51], s[50:51] op_sel_hi:[1,1,0]
	s_nop 0
	v_pk_fma_f32 v[50:51], v[46:47], v[50:51], s[52:53] op_sel_hi:[1,1,0]
	s_nop 0
	v_pk_mul_f32 v[46:47], v[46:47], v[50:51]
	s_nop 0
	v_pk_mul_f32 v[46:47], v[46:47], 0.5 op_sel_hi:[1,0]
	s_nop 0
	v_pk_mul_f32 v[46:47], v[48:49], v[46:47]
	s_nop 0
	v_pk_mul_f32 v[48:49], v[42:43], v[46:47]
	v_pk_fma_f32 v[46:47], v[42:43], v[46:47], v[42:43] neg_lo:[1,0,0] neg_hi:[1,0,0]
	s_nop 0
	v_cndmask_b32_e32 v43, v49, v47, vcc
	v_cmp_le_f32_e32 vcc, 0, v42
	s_nop 1
	v_cndmask_b32_e32 v42, v48, v46, vcc
	v_cvt_pk_f16_f32 v42, v42, v43
	v_mul_f32_e64 v43, |v44|, s1
	v_mul_f32_e32 v47, 0xbfb8aa3b, v43
	v_fma_f32 v46, v43, s33, 1.0
	v_mul_f32_e32 v43, v43, v47
	v_exp_f32_e32 v48, v43
	v_mul_f32_e64 v43, |v45|, s1
	v_fma_f32 v47, v43, s33, 1.0
	v_rcp_f32_e32 v46, v46
	v_rcp_f32_e32 v47, v47
	v_mul_f32_e32 v49, 0xbfb8aa3b, v43
	v_mul_f32_e32 v43, v43, v49
	v_exp_f32_e32 v49, v43
	v_pk_fma_f32 v[50:51], v[46:47], s[0:1], v[70:71] op_sel_hi:[1,0,0]
	v_cmp_le_f32_e32 vcc, 0, v45
	v_pk_fma_f32 v[50:51], v[46:47], v[50:51], s[48:49] op_sel_hi:[1,1,0]
	s_nop 0
	v_pk_fma_f32 v[50:51], v[46:47], v[50:51], s[50:51] op_sel_hi:[1,1,0]
	s_nop 0
	v_pk_fma_f32 v[50:51], v[46:47], v[50:51], s[52:53] op_sel_hi:[1,1,0]
	s_nop 0
	v_pk_mul_f32 v[46:47], v[46:47], v[50:51]
	s_nop 0
	v_pk_mul_f32 v[46:47], v[46:47], 0.5 op_sel_hi:[1,0]
	s_nop 0
	v_pk_mul_f32 v[46:47], v[48:49], v[46:47]
	s_nop 0
	v_pk_mul_f32 v[48:49], v[44:45], v[46:47]
	v_pk_fma_f32 v[46:47], v[44:45], v[46:47], v[44:45] neg_lo:[1,0,0] neg_hi:[1,0,0]
	s_nop 0
	v_cndmask_b32_e32 v43, v49, v47, vcc
	v_cmp_le_f32_e32 vcc, 0, v44
	s_nop 1
	v_cndmask_b32_e32 v44, v48, v46, vcc
	v_cvt_pk_f16_f32 v43, v44, v43
	global_store_dwordx2 v[72:73], v[42:43], off offset:480
	v_or_b32_e32 v42, 0x200, v178
	v_mov_b32_e32 v43, v137
	v_lshl_add_u64 v[42:43], v[182:183], 0, v[42:43]
	s_barrier
	v_or_b32_e32 v42, 0x280, v178
	v_mov_b32_e32 v43, v137
	v_lshl_add_u64 v[42:43], v[182:183], 0, v[42:43]
	v_or_b32_e32 v42, 0x300, v178
	v_mov_b32_e32 v43, v137
	v_lshl_add_u64 v[42:43], v[182:183], 0, v[42:43]
	v_or_b32_e32 v42, 0x380, v178
	v_mov_b32_e32 v43, v137
	v_lshl_add_u64 v[42:43], v[182:183], 0, v[42:43]
	s_mov_b32 s33, s66
	s_and_saveexec_b64 s[0:1], s[38:39]
	s_cbranch_execz .LBB3_36
	s_movk_i32 s38, 0x1ff
	v_cmp_lt_u32_e32 vcc, s38, v0
	s_and_saveexec_b64 s[38:39], vcc
	s_cbranch_execz .LBB3_35
	s_movk_i32 s45, 0x2ff
	v_cmp_lt_u32_e32 vcc, s45, v0
	s_and_saveexec_b64 s[46:47], vcc
	s_xor_b64 s[46:47], exec, s[46:47]
	v_add_u32_e32 v193, 0xf000, v191
	s_andn2_saveexec_b64 s[46:47], s[46:47]
	v_add_u32_e32 v193, 0x10600, v191
	s_or_b64 exec, exec, s[46:47]

.LBB3_44:
	s_or_b64 exec, exec, s[0:1]
	s_waitcnt lgkmcnt(0)
	s_barrier
	global_load_dwordx4 v[42:45], v[180:181], off
	global_load_dwordx4 v[52:55], v[180:181], off offset:16
	global_load_dwordx4 v[118:121], v[180:181], off offset:128
	s_mov_b32 s0, s59
	ds_read_b32 v8, v227
	ds_read_b32 v9, v228
	ds_read_b32 v46, v229
	ds_read_b32 v47, v230
	ds_read_b32 v76, v231
	ds_read_b32 v77, v233
	ds_read_b32 v134, v234
	ds_read_b32 v135, v235
	global_load_dwordx4 v[122:125], v[180:181], off offset:144
	global_load_dwordx4 v[126:129], v[180:181], off offset:256
	global_load_dwordx4 v[130:133], v[180:181], off offset:272
	global_load_dwordx4 v[60:63], v[180:181], off offset:384
	global_load_dwordx4 v[114:117], v[180:181], off offset:400
	global_load_dwordx4 v[110:113], v[180:181], off offset:512
	global_load_dwordx4 v[106:109], v[180:181], off offset:528
	global_load_dwordx4 v[102:105], v[180:181], off offset:640
	global_load_dwordx4 v[98:101], v[180:181], off offset:656
	global_load_dwordx4 v[94:97], v[180:181], off offset:768
	global_load_dwordx4 v[90:93], v[180:181], off offset:784
	global_load_dwordx4 v[4:7], v[180:181], off offset:896
	global_load_dwordx4 v[0:3], v[180:181], off offset:912
	s_waitcnt lgkmcnt(0)
	v_add_f32_e32 v137, s0, v8
	v_add_f32_e32 v140, s0, v9
	v_add_f32_e32 v141, s0, v46
	v_add_f32_e32 v142, s0, v47
	v_add_f32_e32 v143, s0, v76
	v_add_f32_e32 v144, s0, v77
	v_add_f32_e32 v145, s0, v134
	v_add_f32_e32 v146, s0, v135
	v_cndmask_b32_e64 v8, v8, v137, s[18:19]
	v_cndmask_b32_e64 v9, v9, v140, s[20:21]
	v_cndmask_b32_e64 v46, v46, v141, s[22:23]
	v_cndmask_b32_e64 v47, v47, v142, s[24:25]
	v_cndmask_b32_e64 v76, v76, v143, s[26:27]
	v_cndmask_b32_e64 v77, v77, v144, s[28:29]
	v_cndmask_b32_e64 v134, v134, v145, s[30:31]
	v_cndmask_b32_e64 v135, v135, v146, s[34:35]
	v_cvt_pk_f16_f32 v143, v134, v135
	v_cvt_pk_f16_f32 v142, v76, v77
	v_cvt_pk_f16_f32 v141, v46, v47
	v_cvt_pk_f16_f32 v140, v8, v9
	ds_write_b128 v232, v[140:143]
	s_waitcnt lgkmcnt(0)
	s_barrier
	s_mov_b32 s2, s63
	s_mov_b32 s0, s65
	s_waitcnt lgkmcnt(0)
	v_mov_b64_e32 v[8:9], s[2:3]
	s_waitcnt vmcnt(15)
	v_cvt_f32_f16_e32 v47, v43
	v_cvt_f32_f16_e32 v46, v42
	v_cvt_f32_f16_e32 v77, v45
	v_cvt_f32_f16_e32 v76, v44
	s_waitcnt vmcnt(14)
	v_cvt_f32_f16_e32 v135, v53
	v_cvt_f32_f16_e32 v134, v52
	v_cvt_f32_f16_sdwa v43, v43 dst_sel:DWORD dst_unused:UNUSED_PAD src0_sel:WORD_1
	v_cvt_f32_f16_sdwa v42, v42 dst_sel:DWORD dst_unused:UNUSED_PAD src0_sel:WORD_1
	v_cvt_f32_f16_sdwa v45, v45 dst_sel:DWORD dst_unused:UNUSED_PAD src0_sel:WORD_1
	v_cvt_f32_f16_sdwa v44, v44 dst_sel:DWORD dst_unused:UNUSED_PAD src0_sel:WORD_1
	v_cvt_f32_f16_sdwa v53, v53 dst_sel:DWORD dst_unused:UNUSED_PAD src0_sel:WORD_1
	v_cvt_f32_f16_sdwa v52, v52 dst_sel:DWORD dst_unused:UNUSED_PAD src0_sel:WORD_1
	v_cvt_f32_f16_e32 v141, v55
	v_cvt_f32_f16_e32 v140, v54
	v_cvt_f32_f16_sdwa v55, v55 dst_sel:DWORD dst_unused:UNUSED_PAD src0_sel:WORD_1
	v_cvt_f32_f16_sdwa v54, v54 dst_sel:DWORD dst_unused:UNUSED_PAD src0_sel:WORD_1
	s_waitcnt vmcnt(13)
	v_cvt_f32_f16_e32 v143, v119
	v_cvt_f32_f16_e32 v142, v118
	v_pk_add_f32 v[46:47], v[46:47], 1.0 op_sel_hi:[1,0]
	v_pk_add_f32 v[76:77], v[76:77], 1.0 op_sel_hi:[1,0]
	v_pk_add_f32 v[134:135], v[134:135], 1.0 op_sel_hi:[1,0]
	v_cvt_f32_f16_sdwa v119, v119 dst_sel:DWORD dst_unused:UNUSED_PAD src0_sel:WORD_1
	v_pk_add_f32 v[140:141], v[140:141], 1.0 op_sel_hi:[1,0]
	v_pk_fma_f32 v[38:39], v[38:39], v[46:47], v[42:43]
	v_pk_fma_f32 v[40:41], v[40:41], v[76:77], v[44:45]
	v_pk_fma_f32 v[34:35], v[34:35], v[134:135], v[52:53]
	v_cvt_f32_f16_sdwa v118, v118 dst_sel:DWORD dst_unused:UNUSED_PAD src0_sel:WORD_1
	v_pk_fma_f32 v[42:43], v[36:37], v[140:141], v[54:55]
	v_pk_fma_f32 v[36:37], v[38:39], s[0:1], v[8:9] op_sel_hi:[1,0,0]
	v_pk_fma_f32 v[38:39], v[40:41], s[0:1], v[8:9] op_sel_hi:[1,0,0]
	v_pk_fma_f32 v[34:35], v[34:35], s[0:1], v[8:9] op_sel_hi:[1,0,0]
	v_cvt_pk_f16_f32 v36, v36, v37
	v_cvt_pk_f16_f32 v37, v38, v39
	v_cvt_pk_f16_f32 v38, v34, v35
	v_pk_fma_f32 v[34:35], v[42:43], s[0:1], v[8:9] op_sel_hi:[1,0,0]
	v_cvt_f32_f16_sdwa v41, v121 dst_sel:DWORD dst_unused:UNUSED_PAD src0_sel:WORD_1
	v_cvt_pk_f16_f32 v39, v34, v35
	v_pk_add_f32 v[34:35], v[142:143], 1.0 op_sel_hi:[1,0]
	v_cvt_f32_f16_sdwa v40, v120 dst_sel:DWORD dst_unused:UNUSED_PAD src0_sel:WORD_1
	v_pk_fma_f32 v[30:31], v[30:31], v[34:35], v[118:119]
	v_cvt_f32_f16_e32 v35, v121
	v_cvt_f32_f16_e32 v34, v120
	v_pk_fma_f32 v[30:31], v[30:31], s[0:1], v[8:9] op_sel_hi:[1,0,0]
	s_nop 0
	v_cvt_pk_f16_f32 v44, v30, v31
	v_pk_add_f32 v[30:31], v[34:35], 1.0 op_sel_hi:[1,0]
	s_waitcnt vmcnt(12)
	v_cvt_f32_f16_sdwa v35, v123 dst_sel:DWORD dst_unused:UNUSED_PAD src0_sel:WORD_1
	v_pk_fma_f32 v[30:31], v[32:33], v[30:31], v[40:41]
	v_cvt_f32_f16_e32 v33, v123
	v_cvt_f32_f16_e32 v32, v122
	v_cvt_f32_f16_sdwa v34, v122 dst_sel:DWORD dst_unused:UNUSED_PAD src0_sel:WORD_1
	v_pk_fma_f32 v[30:31], v[30:31], s[0:1], v[8:9] op_sel_hi:[1,0,0]
	s_nop 0
	v_cvt_pk_f16_f32 v45, v30, v31
	v_pk_add_f32 v[30:31], v[32:33], 1.0 op_sel_hi:[1,0]
	v_cvt_f32_f16_sdwa v33, v125 dst_sel:DWORD dst_unused:UNUSED_PAD src0_sel:WORD_1
	v_pk_fma_f32 v[26:27], v[26:27], v[30:31], v[34:35]
	v_cvt_f32_f16_e32 v31, v125
	v_cvt_f32_f16_e32 v30, v124
	v_cvt_f32_f16_sdwa v32, v124 dst_sel:DWORD dst_unused:UNUSED_PAD src0_sel:WORD_1
	v_pk_fma_f32 v[26:27], v[26:27], s[0:1], v[8:9] op_sel_hi:[1,0,0]
	s_nop 0
	v_cvt_pk_f16_f32 v46, v26, v27
	v_pk_add_f32 v[26:27], v[30:31], 1.0 op_sel_hi:[1,0]
	s_waitcnt vmcnt(11)
	v_cvt_f32_f16_sdwa v31, v127 dst_sel:DWORD dst_unused:UNUSED_PAD src0_sel:WORD_1
	v_pk_fma_f32 v[26:27], v[28:29], v[26:27], v[32:33]
	v_cvt_f32_f16_e32 v29, v127
	v_cvt_f32_f16_e32 v28, v126
	v_cvt_f32_f16_sdwa v30, v126 dst_sel:DWORD dst_unused:UNUSED_PAD src0_sel:WORD_1
	v_pk_fma_f32 v[26:27], v[26:27], s[0:1], v[8:9] op_sel_hi:[1,0,0]
	s_nop 0
	v_cvt_pk_f16_f32 v47, v26, v27
	v_pk_add_f32 v[26:27], v[28:29], 1.0 op_sel_hi:[1,0]
	v_cvt_f32_f16_sdwa v29, v129 dst_sel:DWORD dst_unused:UNUSED_PAD src0_sel:WORD_1
	v_pk_fma_f32 v[22:23], v[22:23], v[26:27], v[30:31]
	v_cvt_f32_f16_e32 v27, v129
	v_cvt_f32_f16_e32 v26, v128
	v_cvt_f32_f16_sdwa v28, v128 dst_sel:DWORD dst_unused:UNUSED_PAD src0_sel:WORD_1
	v_pk_fma_f32 v[22:23], v[22:23], s[0:1], v[8:9] op_sel_hi:[1,0,0]
	s_nop 0
	v_cvt_pk_f16_f32 v52, v22, v23
	v_pk_add_f32 v[22:23], v[26:27], 1.0 op_sel_hi:[1,0]
	s_waitcnt vmcnt(10)
	v_cvt_f32_f16_sdwa v27, v131 dst_sel:DWORD dst_unused:UNUSED_PAD src0_sel:WORD_1
	v_pk_fma_f32 v[22:23], v[24:25], v[22:23], v[28:29]
	v_cvt_f32_f16_e32 v25, v131
	v_cvt_f32_f16_e32 v24, v130
	v_cvt_f32_f16_sdwa v26, v130 dst_sel:DWORD dst_unused:UNUSED_PAD src0_sel:WORD_1
	v_pk_fma_f32 v[22:23], v[22:23], s[0:1], v[8:9] op_sel_hi:[1,0,0]
	s_nop 0
	v_cvt_pk_f16_f32 v53, v22, v23
	v_pk_add_f32 v[22:23], v[24:25], 1.0 op_sel_hi:[1,0]
	v_cvt_f32_f16_sdwa v25, v133 dst_sel:DWORD dst_unused:UNUSED_PAD src0_sel:WORD_1
	v_pk_fma_f32 v[18:19], v[18:19], v[22:23], v[26:27]
	v_cvt_f32_f16_e32 v23, v133
	v_cvt_f32_f16_e32 v22, v132
	v_cvt_f32_f16_sdwa v24, v132 dst_sel:DWORD dst_unused:UNUSED_PAD src0_sel:WORD_1
	v_pk_fma_f32 v[18:19], v[18:19], s[0:1], v[8:9] op_sel_hi:[1,0,0]
	s_nop 0
	v_cvt_pk_f16_f32 v54, v18, v19
	v_pk_add_f32 v[18:19], v[22:23], 1.0 op_sel_hi:[1,0]
	s_waitcnt vmcnt(9)
	v_cvt_f32_f16_sdwa v23, v61 dst_sel:DWORD dst_unused:UNUSED_PAD src0_sel:WORD_1
	v_pk_fma_f32 v[18:19], v[20:21], v[18:19], v[24:25]
	v_cvt_f32_f16_e32 v21, v61
	v_cvt_f32_f16_e32 v20, v60
	v_cvt_f32_f16_sdwa v22, v60 dst_sel:DWORD dst_unused:UNUSED_PAD src0_sel:WORD_1
	v_pk_fma_f32 v[18:19], v[18:19], s[0:1], v[8:9] op_sel_hi:[1,0,0]
	s_nop 0
	v_cvt_pk_f16_f32 v55, v18, v19
	v_pk_add_f32 v[18:19], v[20:21], 1.0 op_sel_hi:[1,0]
	v_cvt_f32_f16_sdwa v21, v63 dst_sel:DWORD dst_unused:UNUSED_PAD src0_sel:WORD_1
	v_pk_fma_f32 v[14:15], v[14:15], v[18:19], v[22:23]
	v_cvt_f32_f16_e32 v19, v63
	v_cvt_f32_f16_e32 v18, v62
	v_cvt_f32_f16_sdwa v20, v62 dst_sel:DWORD dst_unused:UNUSED_PAD src0_sel:WORD_1
	v_pk_fma_f32 v[14:15], v[14:15], s[0:1], v[8:9] op_sel_hi:[1,0,0]
	s_nop 0
	v_cvt_pk_f16_f32 v60, v14, v15
	v_pk_add_f32 v[14:15], v[18:19], 1.0 op_sel_hi:[1,0]
	s_waitcnt vmcnt(8)
	v_cvt_f32_f16_sdwa v19, v115 dst_sel:DWORD dst_unused:UNUSED_PAD src0_sel:WORD_1
	v_pk_fma_f32 v[14:15], v[16:17], v[14:15], v[20:21]
	v_cvt_f32_f16_e32 v17, v115
	v_cvt_f32_f16_e32 v16, v114
	v_cvt_f32_f16_sdwa v18, v114 dst_sel:DWORD dst_unused:UNUSED_PAD src0_sel:WORD_1
	v_pk_fma_f32 v[14:15], v[14:15], s[0:1], v[8:9] op_sel_hi:[1,0,0]
	s_nop 0
	v_cvt_pk_f16_f32 v61, v14, v15
	v_pk_add_f32 v[14:15], v[16:17], 1.0 op_sel_hi:[1,0]
	v_cvt_f32_f16_sdwa v17, v117 dst_sel:DWORD dst_unused:UNUSED_PAD src0_sel:WORD_1
	v_pk_fma_f32 v[10:11], v[10:11], v[14:15], v[18:19]
	v_cvt_f32_f16_e32 v15, v117
	v_cvt_f32_f16_e32 v14, v116
	v_cvt_f32_f16_sdwa v16, v116 dst_sel:DWORD dst_unused:UNUSED_PAD src0_sel:WORD_1
	v_pk_fma_f32 v[10:11], v[10:11], s[0:1], v[8:9] op_sel_hi:[1,0,0]
	s_nop 0
	v_cvt_pk_f16_f32 v62, v10, v11
	v_pk_add_f32 v[10:11], v[14:15], 1.0 op_sel_hi:[1,0]
	s_waitcnt vmcnt(7)
	v_cvt_f32_f16_sdwa v15, v111 dst_sel:DWORD dst_unused:UNUSED_PAD src0_sel:WORD_1
	v_pk_fma_f32 v[10:11], v[12:13], v[10:11], v[16:17]
	v_cvt_f32_f16_e32 v13, v111
	v_cvt_f32_f16_e32 v12, v110
	v_cvt_f32_f16_sdwa v14, v110 dst_sel:DWORD dst_unused:UNUSED_PAD src0_sel:WORD_1
	v_pk_fma_f32 v[10:11], v[10:11], s[0:1], v[8:9] op_sel_hi:[1,0,0]
	s_nop 0
	v_cvt_pk_f16_f32 v63, v10, v11
	v_pk_add_f32 v[10:11], v[12:13], 1.0 op_sel_hi:[1,0]
	v_cvt_f32_f16_e32 v13, v113
	v_cvt_f32_f16_e32 v12, v112
	v_pk_fma_f32 v[10:11], v[152:153], v[10:11], v[14:15]
	v_cvt_f32_f16_sdwa v15, v113 dst_sel:DWORD dst_unused:UNUSED_PAD src0_sel:WORD_1
	v_cvt_f32_f16_sdwa v14, v112 dst_sel:DWORD dst_unused:UNUSED_PAD src0_sel:WORD_1
	v_pk_fma_f32 v[10:11], v[10:11], s[0:1], v[8:9] op_sel_hi:[1,0,0]
	s_nop 0
	v_cvt_pk_f16_f32 v68, v10, v11
	v_pk_add_f32 v[10:11], v[12:13], 1.0 op_sel_hi:[1,0]
	s_waitcnt vmcnt(6)
	v_cvt_f32_f16_e32 v13, v107
	v_cvt_f32_f16_e32 v12, v106
	v_pk_fma_f32 v[10:11], v[154:155], v[10:11], v[14:15]
	v_cvt_f32_f16_sdwa v15, v107 dst_sel:DWORD dst_unused:UNUSED_PAD src0_sel:WORD_1
	v_cvt_f32_f16_sdwa v14, v106 dst_sel:DWORD dst_unused:UNUSED_PAD src0_sel:WORD_1
	v_pk_fma_f32 v[10:11], v[10:11], s[0:1], v[8:9] op_sel_hi:[1,0,0]
	s_nop 0
	v_cvt_pk_f16_f32 v69, v10, v11
	v_pk_add_f32 v[10:11], v[12:13], 1.0 op_sel_hi:[1,0]
	v_cvt_f32_f16_e32 v13, v109
	v_cvt_f32_f16_e32 v12, v108
	v_pk_fma_f32 v[10:11], v[148:149], v[10:11], v[14:15]
	v_cvt_f32_f16_sdwa v15, v109 dst_sel:DWORD dst_unused:UNUSED_PAD src0_sel:WORD_1
	v_cvt_f32_f16_sdwa v14, v108 dst_sel:DWORD dst_unused:UNUSED_PAD src0_sel:WORD_1
	v_pk_fma_f32 v[10:11], v[10:11], s[0:1], v[8:9] op_sel_hi:[1,0,0]
	s_nop 0
	v_cvt_pk_f16_f32 v70, v10, v11
	v_pk_add_f32 v[10:11], v[12:13], 1.0 op_sel_hi:[1,0]
	s_waitcnt vmcnt(5)
	v_cvt_f32_f16_e32 v13, v103
	v_cvt_f32_f16_e32 v12, v102
	v_pk_fma_f32 v[10:11], v[150:151], v[10:11], v[14:15]
	v_cvt_f32_f16_sdwa v15, v103 dst_sel:DWORD dst_unused:UNUSED_PAD src0_sel:WORD_1
	v_cvt_f32_f16_sdwa v14, v102 dst_sel:DWORD dst_unused:UNUSED_PAD src0_sel:WORD_1
	v_pk_fma_f32 v[10:11], v[10:11], s[0:1], v[8:9] op_sel_hi:[1,0,0]
	s_nop 0
	v_cvt_pk_f16_f32 v71, v10, v11
	v_pk_add_f32 v[10:11], v[12:13], 1.0 op_sel_hi:[1,0]
	v_cvt_f32_f16_e32 v13, v105
	v_cvt_f32_f16_e32 v12, v104
	v_pk_fma_f32 v[10:11], v[160:161], v[10:11], v[14:15]
	v_cvt_f32_f16_sdwa v15, v105 dst_sel:DWORD dst_unused:UNUSED_PAD src0_sel:WORD_1
	v_cvt_f32_f16_sdwa v14, v104 dst_sel:DWORD dst_unused:UNUSED_PAD src0_sel:WORD_1
	v_pk_fma_f32 v[10:11], v[10:11], s[0:1], v[8:9] op_sel_hi:[1,0,0]
	s_nop 0
	v_cvt_pk_f16_f32 v76, v10, v11
	v_pk_add_f32 v[10:11], v[12:13], 1.0 op_sel_hi:[1,0]
	s_waitcnt vmcnt(4)
	v_cvt_f32_f16_e32 v13, v99
	v_cvt_f32_f16_e32 v12, v98
	v_pk_fma_f32 v[10:11], v[162:163], v[10:11], v[14:15]
	v_cvt_f32_f16_sdwa v15, v99 dst_sel:DWORD dst_unused:UNUSED_PAD src0_sel:WORD_1
	v_cvt_f32_f16_sdwa v14, v98 dst_sel:DWORD dst_unused:UNUSED_PAD src0_sel:WORD_1
	v_pk_fma_f32 v[10:11], v[10:11], s[0:1], v[8:9] op_sel_hi:[1,0,0]
	s_nop 0
	v_cvt_pk_f16_f32 v77, v10, v11
	v_pk_add_f32 v[10:11], v[12:13], 1.0 op_sel_hi:[1,0]
	v_cvt_f32_f16_e32 v13, v101
	v_cvt_f32_f16_e32 v12, v100
	v_pk_fma_f32 v[10:11], v[156:157], v[10:11], v[14:15]
	v_cvt_f32_f16_sdwa v15, v101 dst_sel:DWORD dst_unused:UNUSED_PAD src0_sel:WORD_1
	v_cvt_f32_f16_sdwa v14, v100 dst_sel:DWORD dst_unused:UNUSED_PAD src0_sel:WORD_1
	v_pk_fma_f32 v[10:11], v[10:11], s[0:1], v[8:9] op_sel_hi:[1,0,0]
	s_nop 0
	v_cvt_pk_f16_f32 v78, v10, v11
	v_pk_add_f32 v[10:11], v[12:13], 1.0 op_sel_hi:[1,0]
	s_waitcnt vmcnt(3)
	v_cvt_f32_f16_e32 v13, v95
	v_cvt_f32_f16_e32 v12, v94
	v_pk_fma_f32 v[10:11], v[158:159], v[10:11], v[14:15]
	v_cvt_f32_f16_sdwa v15, v95 dst_sel:DWORD dst_unused:UNUSED_PAD src0_sel:WORD_1
	v_cvt_f32_f16_sdwa v14, v94 dst_sel:DWORD dst_unused:UNUSED_PAD src0_sel:WORD_1
	v_pk_fma_f32 v[10:11], v[10:11], s[0:1], v[8:9] op_sel_hi:[1,0,0]
	s_nop 0
	v_cvt_pk_f16_f32 v79, v10, v11
	v_pk_add_f32 v[10:11], v[12:13], 1.0 op_sel_hi:[1,0]
	v_cvt_f32_f16_e32 v13, v97
	v_cvt_f32_f16_e32 v12, v96
	v_pk_fma_f32 v[10:11], v[168:169], v[10:11], v[14:15]
	v_cvt_f32_f16_sdwa v15, v97 dst_sel:DWORD dst_unused:UNUSED_PAD src0_sel:WORD_1
	v_cvt_f32_f16_sdwa v14, v96 dst_sel:DWORD dst_unused:UNUSED_PAD src0_sel:WORD_1
	v_pk_fma_f32 v[10:11], v[10:11], s[0:1], v[8:9] op_sel_hi:[1,0,0]
	s_nop 0
	v_cvt_pk_f16_f32 v84, v10, v11
	v_pk_add_f32 v[10:11], v[12:13], 1.0 op_sel_hi:[1,0]
	s_waitcnt vmcnt(2)
	v_cvt_f32_f16_e32 v13, v91
	v_cvt_f32_f16_e32 v12, v90
	v_pk_fma_f32 v[10:11], v[170:171], v[10:11], v[14:15]
	v_cvt_f32_f16_sdwa v15, v91 dst_sel:DWORD dst_unused:UNUSED_PAD src0_sel:WORD_1
	v_cvt_f32_f16_sdwa v14, v90 dst_sel:DWORD dst_unused:UNUSED_PAD src0_sel:WORD_1
	v_pk_fma_f32 v[10:11], v[10:11], s[0:1], v[8:9] op_sel_hi:[1,0,0]
	s_nop 0
	v_cvt_pk_f16_f32 v85, v10, v11
	v_pk_add_f32 v[10:11], v[12:13], 1.0 op_sel_hi:[1,0]
	v_cvt_f32_f16_e32 v13, v93
	v_cvt_f32_f16_e32 v12, v92
	v_pk_fma_f32 v[10:11], v[164:165], v[10:11], v[14:15]
	v_cvt_f32_f16_sdwa v15, v93 dst_sel:DWORD dst_unused:UNUSED_PAD src0_sel:WORD_1
	v_cvt_f32_f16_sdwa v14, v92 dst_sel:DWORD dst_unused:UNUSED_PAD src0_sel:WORD_1
	v_pk_fma_f32 v[10:11], v[10:11], s[0:1], v[8:9] op_sel_hi:[1,0,0]
	s_nop 0
	v_cvt_pk_f16_f32 v86, v10, v11
	v_pk_add_f32 v[10:11], v[12:13], 1.0 op_sel_hi:[1,0]
	s_waitcnt vmcnt(1)
	v_cvt_f32_f16_e32 v13, v5
	v_cvt_f32_f16_e32 v12, v4
	v_cvt_f32_f16_sdwa v5, v5 dst_sel:DWORD dst_unused:UNUSED_PAD src0_sel:WORD_1
	v_cvt_f32_f16_sdwa v4, v4 dst_sel:DWORD dst_unused:UNUSED_PAD src0_sel:WORD_1
	v_pk_fma_f32 v[10:11], v[166:167], v[10:11], v[14:15]
	s_nop 0
	v_pk_fma_f32 v[10:11], v[10:11], s[0:1], v[8:9] op_sel_hi:[1,0,0]
	s_nop 0
	v_cvt_pk_f16_f32 v87, v10, v11
	v_pk_add_f32 v[10:11], v[12:13], 1.0 op_sel_hi:[1,0]
	s_nop 0
	v_pk_fma_f32 v[4:5], v[240:241], v[10:11], v[4:5]
	v_cvt_f32_f16_e32 v11, v7
	v_cvt_f32_f16_e32 v10, v6
	v_cvt_f32_f16_sdwa v7, v7 dst_sel:DWORD dst_unused:UNUSED_PAD src0_sel:WORD_1
	v_cvt_f32_f16_sdwa v6, v6 dst_sel:DWORD dst_unused:UNUSED_PAD src0_sel:WORD_1
	v_pk_fma_f32 v[4:5], v[4:5], s[0:1], v[8:9] op_sel_hi:[1,0,0]
	s_nop 0
	v_cvt_pk_f16_f32 v92, v4, v5
	v_pk_add_f32 v[4:5], v[10:11], 1.0 op_sel_hi:[1,0]
	s_nop 0
	v_pk_fma_f32 v[4:5], v[242:243], v[4:5], v[6:7]
	s_waitcnt vmcnt(0)
	v_cvt_f32_f16_e32 v7, v1
	v_cvt_f32_f16_e32 v6, v0
	v_cvt_f32_f16_sdwa v1, v1 dst_sel:DWORD dst_unused:UNUSED_PAD src0_sel:WORD_1
	v_cvt_f32_f16_sdwa v0, v0 dst_sel:DWORD dst_unused:UNUSED_PAD src0_sel:WORD_1
	v_pk_fma_f32 v[4:5], v[4:5], s[0:1], v[8:9] op_sel_hi:[1,0,0]
	s_nop 0
	v_cvt_pk_f16_f32 v93, v4, v5
	v_pk_add_f32 v[4:5], v[6:7], 1.0 op_sel_hi:[1,0]
	s_nop 0
	v_pk_fma_f32 v[0:1], v[184:185], v[4:5], v[0:1]
	v_cvt_f32_f16_e32 v5, v3
	v_cvt_f32_f16_e32 v4, v2
	v_cvt_f32_f16_sdwa v3, v3 dst_sel:DWORD dst_unused:UNUSED_PAD src0_sel:WORD_1
	v_cvt_f32_f16_sdwa v2, v2 dst_sel:DWORD dst_unused:UNUSED_PAD src0_sel:WORD_1
	v_pk_fma_f32 v[0:1], v[0:1], s[0:1], v[8:9] op_sel_hi:[1,0,0]
	s_nop 0
	v_cvt_pk_f16_f32 v94, v0, v1
	v_pk_add_f32 v[0:1], v[4:5], 1.0 op_sel_hi:[1,0]
	s_nop 0
	v_pk_fma_f32 v[0:1], v[186:187], v[0:1], v[2:3]
	s_nop 0
	v_pk_fma_f32 v[0:1], v[0:1], s[0:1], v[8:9] op_sel_hi:[1,0,0]
	s_nop 0
	v_cvt_pk_f16_f32 v95, v0, v1
	ds_read_b128 v[0:3], v236
	ds_read_b128 v[4:7], v236 offset:2048
	ds_read_b128 v[20:23], v237
	ds_read_b128 v[24:27], v237 offset:2048
	s_mov_b32 s0, 0
	v_mov_b32_e32 v137, v179
	s_waitcnt lgkmcnt(3)
	v_mfma_f32_16x16x32_f16 v[8:11], v[0:3], v[36:39], 0
	v_mfma_f32_16x16x32_f16 v[12:15], v[0:3], v[52:55], 0
	v_mfma_f32_16x16x32_f16 v[16:19], v[0:3], v[68:71], 0
	v_mfma_f32_16x16x32_f16 v[0:3], v[0:3], v[84:87], 0
	s_waitcnt lgkmcnt(1)
	v_mfma_f32_16x16x32_f16 v[88:91], v[20:23], v[44:47], v[8:11]
	v_mfma_f32_16x16x32_f16 v[80:83], v[20:23], v[60:63], v[12:15]
	v_mfma_f32_16x16x32_f16 v[64:67], v[20:23], v[92:95], v[0:3]
	v_mfma_f32_16x16x32_f16 v[0:3], v[4:7], v[36:39], 0
	v_mfma_f32_16x16x32_f16 v[8:11], v[4:7], v[52:55], 0
	v_mfma_f32_16x16x32_f16 v[12:15], v[4:7], v[68:71], 0
	v_mfma_f32_16x16x32_f16 v[4:7], v[4:7], v[84:87], 0
	s_waitcnt lgkmcnt(0)
	v_mfma_f32_16x16x32_f16 v[56:59], v[24:27], v[44:47], v[0:3]
	v_mfma_f32_16x16x32_f16 v[32:35], v[24:27], v[92:95], v[4:7]
	s_nop 1
	ds_read_b128 v[0:3], v236 offset:4096
	s_nop 1
	ds_read_b128 v[4:7], v236 offset:6144
	ds_read_b128 v[96:99], v237 offset:4096
	ds_read_b128 v[100:103], v237 offset:6144
	v_mfma_f32_16x16x32_f16 v[72:75], v[20:23], v[76:79], v[16:19]
	v_mfma_f32_16x16x32_f16 v[48:51], v[24:27], v[60:63], v[8:11]
	v_mfma_f32_16x16x32_f16 v[40:43], v[24:27], v[76:79], v[12:15]
	s_waitcnt lgkmcnt(3)
	v_mfma_f32_16x16x32_f16 v[8:11], v[0:3], v[36:39], 0
	v_mfma_f32_16x16x32_f16 v[12:15], v[0:3], v[52:55], 0
	v_mfma_f32_16x16x32_f16 v[16:19], v[0:3], v[68:71], 0
	v_mfma_f32_16x16x32_f16 v[0:3], v[0:3], v[84:87], 0
	s_waitcnt lgkmcnt(1)
	v_mfma_f32_16x16x32_f16 v[28:31], v[96:99], v[44:47], v[8:11]
	v_mfma_f32_16x16x32_f16 v[24:27], v[96:99], v[60:63], v[12:15]
	v_mfma_f32_16x16x32_f16 v[20:23], v[96:99], v[76:79], v[16:19]
	v_mfma_f32_16x16x32_f16 v[16:19], v[96:99], v[92:95], v[0:3]
	v_mfma_f32_16x16x32_f16 v[0:3], v[4:7], v[36:39], 0
	v_mfma_f32_16x16x32_f16 v[8:11], v[4:7], v[52:55], 0
	v_mfma_f32_16x16x32_f16 v[96:99], v[4:7], v[68:71], 0
	v_mfma_f32_16x16x32_f16 v[104:107], v[4:7], v[84:87], 0
	s_waitcnt lgkmcnt(0)
	v_mfma_f32_16x16x32_f16 v[12:15], v[100:103], v[44:47], v[0:3]
	v_mfma_f32_16x16x32_f16 v[8:11], v[100:103], v[60:63], v[8:11]
	v_mfma_f32_16x16x32_f16 v[4:7], v[100:103], v[76:79], v[96:99]
	v_mfma_f32_16x16x32_f16 v[0:3], v[100:103], v[92:95], v[104:107]

	.amdhsa_kernel _Z5k_ssdPKfPKDv2_DF16_S0_S0_S0_S0_S0_PDF16_
		.amdhsa_group_segment_fixed_size 0
		.amdhsa_private_segment_fixed_size 0
		.amdhsa_kernarg_size 64
		.amdhsa_user_sgpr_count 2
		.amdhsa_user_sgpr_dispatch_ptr 0
		.amdhsa_user_sgpr_queue_ptr 0
		.amdhsa_user_sgpr_kernarg_segment_ptr 1
		.amdhsa_user_sgpr_dispatch_id 0
		.amdhsa_user_sgpr_kernarg_preload_length 0
		.amdhsa_user_sgpr_kernarg_preload_offset 0
		.amdhsa_user_sgpr_private_segment_size 0
		.amdhsa_uses_dynamic_stack 0
		.amdhsa_enable_private_segment 0
		.amdhsa_system_sgpr_workgroup_id_x 1
		.amdhsa_system_sgpr_workgroup_id_y 0
		.amdhsa_system_sgpr_workgroup_id_z 0
		.amdhsa_system_sgpr_workgroup_info 0
		.amdhsa_system_vgpr_workitem_id 0
		.amdhsa_next_free_vgpr 256
		.amdhsa_next_free_sgpr 70
		.amdhsa_accum_offset 256
		.amdhsa_reserve_vcc 1
		.amdhsa_float_round_mode_32 0
		.amdhsa_float_round_mode_16_64 0
		.amdhsa_float_denorm_mode_32 3
		.amdhsa_float_denorm_mode_16_64 3
		.amdhsa_dx10_clamp 1
		.amdhsa_ieee_mode 1
		.amdhsa_fp16_overflow 0
		.amdhsa_tg_split 0
		.amdhsa_exception_fp_ieee_invalid_op 0
		.amdhsa_exception_fp_denorm_src 0
		.amdhsa_exception_fp_ieee_div_zero 0
		.amdhsa_exception_fp_ieee_overflow 0
		.amdhsa_exception_fp_ieee_underflow 0
		.amdhsa_exception_fp_ieee_inexact 0
		.amdhsa_exception_int_div_zero 0
	.end_amdhsa_kernel

amdhsa.kernels:
  - .agpr_count:     0
    .args:
      - .actual_access:  read_only
        .address_space:  global
        .offset:         0
        .size:           8
        .value_kind:     global_buffer
      - .actual_access:  write_only
        .address_space:  global
        .offset:         8
        .size:           8
        .value_kind:     global_buffer
      - .actual_access:  read_only
        .address_space:  global
        .offset:         16
        .size:           8
        .value_kind:     global_buffer
      - .actual_access:  write_only
        .address_space:  global
        .offset:         24
        .size:           8
        .value_kind:     global_buffer
      - .actual_access:  read_only
        .address_space:  global
        .offset:         32
        .size:           8
        .value_kind:     global_buffer
      - .actual_access:  read_only
        .address_space:  global
        .offset:         40
        .size:           8
        .value_kind:     global_buffer
      - .actual_access:  read_only
        .address_space:  global
        .offset:         48
        .size:           8
        .value_kind:     global_buffer
      - .actual_access:  read_only
        .address_space:  global
        .offset:         56
        .size:           8
        .value_kind:     global_buffer
      - .actual_access:  read_only
        .address_space:  global
        .offset:         64
        .size:           8
        .value_kind:     global_buffer
      - .actual_access:  read_only
        .address_space:  global
        .offset:         72
        .size:           8
        .value_kind:     global_buffer
      - .actual_access:  write_only
        .address_space:  global
        .offset:         80
        .size:           8
        .value_kind:     global_buffer
    .group_segment_fixed_size: 8192
    .kernarg_segment_align: 8
    .kernarg_segment_size: 88
    .language:       OpenCL C
    .language_version:
      - 2
      - 0
    .max_flat_workgroup_size: 256
    .name:           _Z7k_statsPKfPDv2_DF16_S0_PDF16_S0_S0_S0_S0_S0_S0_Pf
    .private_segment_fixed_size: 0
    .sgpr_count:     51
    .sgpr_spill_count: 0
    .symbol:         _Z7k_statsPKfPDv2_DF16_S0_PDF16_S0_S0_S0_S0_S0_S0_Pf.kd
    .uniform_work_group_size: 1
    .uses_dynamic_stack: false
    .vgpr_count:     64
    .vgpr_spill_count: 0
    .wavefront_size: 64
  - .agpr_count:     0
    .args:
      - .actual_access:  read_only
        .address_space:  global
        .offset:         0
        .size:           8
        .value_kind:     global_buffer
      - .actual_access:  read_only
        .address_space:  global
        .offset:         8
        .size:           8
        .value_kind:     global_buffer
      - .actual_access:  read_only
        .address_space:  global
        .offset:         16
        .size:           8
        .value_kind:     global_buffer
      - .actual_access:  read_only
        .address_space:  global
        .offset:         24
        .size:           8
        .value_kind:     global_buffer
      - .actual_access:  write_only
        .address_space:  global
        .offset:         32
        .size:           8
        .value_kind:     global_buffer
    .group_segment_fixed_size: 0
    .kernarg_segment_align: 8
    .kernarg_segment_size: 40
    .language:       OpenCL C
    .language_version:
      - 2
      - 0
    .max_flat_workgroup_size: 256
    .name:           _Z6k_normPKfPK15HIP_vector_typeIfLj2EES0_S0_PDF16_
    .private_segment_fixed_size: 0
    .sgpr_count:     36
    .sgpr_spill_count: 0
    .symbol:         _Z6k_normPKfPK15HIP_vector_typeIfLj2EES0_S0_PDF16_.kd
    .uniform_work_group_size: 1
    .uses_dynamic_stack: false
    .vgpr_count:     66
    .vgpr_spill_count: 0
    .wavefront_size: 64
  - .agpr_count:     0
    .args:
      - .actual_access:  read_only
        .address_space:  global
        .offset:         0
        .size:           8
        .value_kind:     global_buffer
      - .actual_access:  write_only
        .address_space:  global
        .offset:         8
        .size:           8
        .value_kind:     global_buffer
    .group_segment_fixed_size: 0
    .kernarg_segment_align: 8
    .kernarg_segment_size: 16
    .language:       OpenCL C
    .language_version:
      - 2
      - 0
    .max_flat_workgroup_size: 256
    .name:           _Z5k_finPK15HIP_vector_typeIfLj2EEPDv2_DF16_
    .private_segment_fixed_size: 0
    .sgpr_count:     14
    .sgpr_spill_count: 0
    .symbol:         _Z5k_finPK15HIP_vector_typeIfLj2EEPDv2_DF16_.kd
    .uniform_work_group_size: 1
    .uses_dynamic_stack: false
    .vgpr_count:     18
    .vgpr_spill_count: 0
    .wavefront_size: 64
  - .agpr_count:     0
    .args:
      - .actual_access:  read_only
        .address_space:  global
        .offset:         0
        .size:           8
        .value_kind:     global_buffer
      - .actual_access:  read_only
        .address_space:  global
        .offset:         8
        .size:           8
        .value_kind:     global_buffer
      - .actual_access:  read_only
        .address_space:  global
        .offset:         16
        .size:           8
        .value_kind:     global_buffer
      - .actual_access:  read_only
        .address_space:  global
        .offset:         24
        .size:           8
        .value_kind:     global_buffer
      - .actual_access:  read_only
        .address_space:  global
        .offset:         32
        .size:           8
        .value_kind:     global_buffer
      - .actual_access:  read_only
        .address_space:  global
        .offset:         40
        .size:           8
        .value_kind:     global_buffer
      - .actual_access:  read_only
        .address_space:  global
        .offset:         48
        .size:           8
        .value_kind:     global_buffer
      - .address_space:  global
        .offset:         56
        .size:           8
        .value_kind:     global_buffer
    .group_segment_fixed_size: 0
    .kernarg_segment_align: 8
    .kernarg_segment_size: 64
    .language:       OpenCL C
    .language_version:
      - 2
      - 0
    .max_flat_workgroup_size: 512
    .name:           _Z5k_ssdPKfPKDv2_DF16_S0_S0_S0_S0_S0_PDF16_
    .private_segment_fixed_size: 0
    .sgpr_count:     76
    .sgpr_spill_count: 0
    .symbol:         _Z5k_ssdPKfPKDv2_DF16_S0_S0_S0_S0_S0_PDF16_.kd
    .uniform_work_group_size: 1
    .uses_dynamic_stack: false
    .vgpr_count:     256
    .vgpr_spill_count: 0
    .wavefront_size: 64
  - .agpr_count:     0
    .args:
      - .actual_access:  read_only
        .address_space:  global
        .offset:         0
        .size:           8
        .value_kind:     global_buffer
      - .actual_access:  write_only
        .address_space:  global
        .offset:         8
        .size:           8
        .value_kind:     global_buffer
    .group_segment_fixed_size: 0
    .kernarg_segment_align: 8
    .kernarg_segment_size: 16
    .language:       OpenCL C
    .language_version:
      - 2
      - 0
    .max_flat_workgroup_size: 256
    .name:           _Z7k_wprepPKfPDF16_
    .private_segment_fixed_size: 0
    .sgpr_count:     14
    .sgpr_spill_count: 0
    .symbol:         _Z7k_wprepPKfPDF16_.kd
    .uniform_work_group_size: 1
    .uses_dynamic_stack: false
    .vgpr_count:     15
    .vgpr_spill_count: 0
    .wavefront_size: 64
  - .agpr_count:     0
    .args:
      - .actual_access:  read_only
        .address_space:  global
        .offset:         0
        .size:           8
        .value_kind:     global_buffer
      - .actual_access:  read_only
        .address_space:  global
        .offset:         8
        .size:           8
        .value_kind:     global_buffer
      - .actual_access:  read_only
        .address_space:  global
        .offset:         16
        .size:           8
        .value_kind:     global_buffer
      - .actual_access:  write_only
        .address_space:  global
        .offset:         24
        .size:           8
        .value_kind:     global_buffer
    .group_segment_fixed_size: 0
    .kernarg_segment_align: 8
    .kernarg_segment_size: 32
    .language:       OpenCL C
    .language_version:
      - 2
      - 0
    .max_flat_workgroup_size: 256
    .name:           _Z6k_gemmPKDF16_S0_PKfPf
    .private_segment_fixed_size: 0
    .sgpr_count:     24
    .sgpr_spill_count: 0
    .symbol:         _Z6k_gemmPKDF16_S0_PKfPf.kd
    .uniform_work_group_size: 1
    .uses_dynamic_stack: false
    .vgpr_count:     139
    .vgpr_spill_count: 0
    .wavefront_size: 64
  - .agpr_count:     0
    .args:
      - .actual_access:  read_only
        .address_space:  global
        .offset:         0
        .size:           8
        .value_kind:     global_buffer
      - .actual_access:  read_only
        .address_space:  global
        .offset:         8
        .size:           8
        .value_kind:     global_buffer
      - .actual_access:  read_only
        .address_space:  global
        .offset:         16
        .size:           8
        .value_kind:     global_buffer
      - .actual_access:  write_only
        .address_space:  global
        .offset:         24
        .size:           8
        .value_kind:     global_buffer
    .group_segment_fixed_size: 0
    .kernarg_segment_align: 8
    .kernarg_segment_size: 32
    .language:       OpenCL C
    .language_version:
      - 2
      - 0
    .max_flat_workgroup_size: 512
    .name:           _Z7k_gemm2PKDF16_S0_PKfPf
    .private_segment_fixed_size: 0
    .sgpr_count:     23
    .sgpr_spill_count: 0
    .symbol:         _Z7k_gemm2PKDF16_S0_PKfPf.kd
    .uniform_work_group_size: 1
    .uses_dynamic_stack: false
    .vgpr_count:     202
    .vgpr_spill_count: 0
    .wavefront_size: 64
  - .agpr_count:     0
    .args:
      - .address_space:  global
        .offset:         0
        .size:           8
        .value_kind:     global_buffer
      - .address_space:  global
        .offset:         8
        .size:           8
        .value_kind:     global_buffer
      - .actual_access:  read_only
        .address_space:  global
        .offset:         16
        .size:           8
        .value_kind:     global_buffer
      - .actual_access:  write_only
        .address_space:  global
        .offset:         24
        .size:           8
        .value_kind:     global_buffer
    .group_segment_fixed_size: 0
    .kernarg_segment_align: 8
    .kernarg_segment_size: 32
    .language:       OpenCL C
    .language_version:
      - 2
      - 0
    .max_flat_workgroup_size: 512
    .name:           _Z7k_gemm3PKDF16_S0_PKfPf
    .private_segment_fixed_size: 0
    .sgpr_count:     49
    .sgpr_spill_count: 0
    .symbol:         _Z7k_gemm3PKDF16_S0_PKfPf.kd
    .uniform_work_group_size: 1
    .uses_dynamic_stack: false
    .vgpr_count:     254
    .vgpr_spill_count: 0
    .wavefront_size: 64
  - .agpr_count:     0
    .args:
      - .address_space:  global
        .offset:         0
        .size:           8
        .value_kind:     global_buffer
      - .address_space:  global
        .offset:         8
        .size:           8
        .value_kind:     global_buffer
      - .actual_access:  read_only
        .address_space:  global
        .offset:         16
        .size:           8
        .value_kind:     global_buffer
      - .actual_access:  write_only
        .address_space:  global
        .offset:         24
        .size:           8
        .value_kind:     global_buffer
    .group_segment_fixed_size: 0
    .kernarg_segment_align: 8
    .kernarg_segment_size: 32
    .language:       OpenCL C
    .language_version:
      - 2
      - 0
    .max_flat_workgroup_size: 256
    .name:           _Z7k_gemm5PKDF16_S0_PKfPf
    .private_segment_fixed_size: 0
    .sgpr_count:     43
    .sgpr_spill_count: 0
    .symbol:         _Z7k_gemm5PKDF16_S0_PKfPf.kd
    .uniform_work_group_size: 1
    .uses_dynamic_stack: false
    .vgpr_count:     190
    .vgpr_spill_count: 0
    .wavefront_size: 64
